# peel+nt plus norm1 parameter loads de-serialised (16 g/scale loads issued up front, one round trip instead of four)
# speedup vs baseline: 1.0065x; 1.0026x over previous
.LBB0_218:
	s_ashr_i32 s0, s38, 31
	s_lshr_b32 s0, s0, 20
	s_add_i32 s0, s38, s0
	s_ashr_i32 s0, s0, 12
	s_mul_hi_i32 s1, s0, 0xc000
	s_mul_i32 s0, s0, 0xc000
	s_add_u32 s2, s25, s0
	s_addc_u32 s3, s34, s1
	global_load_dwordx4 v[8:11], v[112:113], off offset:16
	global_load_dwordx4 v[0:3], v[112:113], off
	global_load_dwordx4 v[12:15], v167, s[2:3] offset:16
	global_load_dwordx4 v[4:7], v167, s[2:3]
	global_load_dwordx4 v[48:51], v[112:113], off offset:2064
	global_load_dwordx4 v[40:43], v[112:113], off offset:2048
	global_load_dwordx4 v[52:55], v167, s[2:3] offset:2064
	global_load_dwordx4 v[44:47], v167, s[2:3] offset:2048
	global_load_dwordx4 v[64:67], v[114:115], off offset:16
	global_load_dwordx4 v[56:59], v[114:115], off
	global_load_dwordx4 v[68:71], v168, s[2:3] offset:16
	global_load_dwordx4 v[60:63], v168, s[2:3]
	global_load_dwordx4 v[80:83], v[116:117], off offset:16
	global_load_dwordx4 v[72:75], v[116:117], off
	global_load_dwordx4 v[84:87], v169, s[2:3] offset:16
	global_load_dwordx4 v[76:79], v169, s[2:3]
	s_add_u32 s0, s23, s0
	s_addc_u32 s1, s24, s1
	s_waitcnt vmcnt(12)
	v_pk_add_f32 v[14:15], v[14:15], 1.0 op_sel_hi:[1,0]
	v_pk_add_f32 v[6:7], v[6:7], 1.0 op_sel_hi:[1,0]
	v_pk_add_f32 v[4:5], v[4:5], 1.0 op_sel_hi:[1,0]
	v_pk_add_f32 v[12:13], v[12:13], 1.0 op_sel_hi:[1,0]
	v_pk_mul_f32 v[128:129], v[2:3], v[6:7]
	v_pk_mul_f32 v[130:131], v[0:1], v[4:5]
	v_pk_mul_f32 v[132:133], v[10:11], v[14:15]
	v_pk_mul_f32 v[134:135], v[8:9], v[12:13]
	global_load_dwordx4 v[0:3], v167, s[0:1] offset:16
	global_load_dwordx4 v[4:7], v167, s[0:1]
	s_waitcnt vmcnt(10)
	v_pk_add_f32 v[54:55], v[54:55], 1.0 op_sel_hi:[1,0]
	v_pk_add_f32 v[46:47], v[46:47], 1.0 op_sel_hi:[1,0]
	v_pk_add_f32 v[44:45], v[44:45], 1.0 op_sel_hi:[1,0]
	v_pk_add_f32 v[52:53], v[52:53], 1.0 op_sel_hi:[1,0]
	v_pk_mul_f32 v[136:137], v[42:43], v[46:47]
	v_pk_mul_f32 v[138:139], v[40:41], v[44:45]
	v_pk_mul_f32 v[140:141], v[50:51], v[54:55]
	v_pk_mul_f32 v[142:143], v[48:49], v[52:53]
	global_load_dwordx4 v[8:11], v167, s[0:1] offset:2064
	global_load_dwordx4 v[12:15], v167, s[0:1] offset:2048
	s_waitcnt vmcnt(8)
	v_pk_add_f32 v[70:71], v[70:71], 1.0 op_sel_hi:[1,0]
	v_pk_add_f32 v[62:63], v[62:63], 1.0 op_sel_hi:[1,0]
	v_pk_add_f32 v[60:61], v[60:61], 1.0 op_sel_hi:[1,0]
	v_pk_add_f32 v[68:69], v[68:69], 1.0 op_sel_hi:[1,0]
	v_pk_mul_f32 v[144:145], v[58:59], v[62:63]
	v_pk_mul_f32 v[146:147], v[56:57], v[60:61]
	v_pk_mul_f32 v[148:149], v[66:67], v[70:71]
	v_pk_mul_f32 v[150:151], v[64:65], v[68:69]
	global_load_dwordx4 v[16:19], v168, s[0:1] offset:16
	global_load_dwordx4 v[20:23], v168, s[0:1]
	s_waitcnt vmcnt(6)
	v_pk_add_f32 v[84:85], v[84:85], 1.0 op_sel_hi:[1,0]
	v_pk_add_f32 v[78:79], v[78:79], 1.0 op_sel_hi:[1,0]
	v_pk_add_f32 v[76:77], v[76:77], 1.0 op_sel_hi:[1,0]
	v_pk_add_f32 v[86:87], v[86:87], 1.0 op_sel_hi:[1,0]
	v_pk_mul_f32 v[152:153], v[74:75], v[78:79]
	v_pk_mul_f32 v[154:155], v[72:73], v[76:77]
	v_pk_mul_f32 v[158:159], v[80:81], v[84:85]
	v_pk_mul_f32 v[156:157], v[82:83], v[86:87]
	global_load_dwordx4 v[24:27], v169, s[0:1] offset:16
	global_load_dwordx4 v[28:31], v169, s[0:1]
	s_ashr_i32 s0, s38, 4
	s_ashr_i32 s1, s0, 31
	s_lshl_b64 s[0:1], s[0:1], 16
	s_add_u32 s2, s20, s0
	s_addc_u32 s3, s21, s1
	s_and_b32 s0, s35, 0x100
	v_or_b32_e32 v32, s0, v166
	v_lshlrev_b32_e32 v212, 1, v32
	v_lshl_add_u64 v[44:45], s[2:3], 0, v[212:213]
	v_lshl_add_u64 v[80:81], v[44:45], 0, v[118:119]
	global_load_dwordx4 v[32:35], v[80:81], off
	v_lshl_add_u64 v[82:83], v[44:45], 0, v[120:121]
	global_load_dwordx4 v[36:39], v[82:83], off
	v_lshl_add_u64 v[84:85], v[44:45], 0, v[122:123]
	global_load_dwordx4 v[40:43], v[84:85], off
	v_lshl_add_u64 v[160:161], v[44:45], 0, v[124:125]
	global_load_dwordx4 v[44:47], v[160:161], off
	global_load_dwordx4 v[76:79], v[80:81], off offset:64
	global_load_dwordx4 v[72:75], v[82:83], off offset:64
	global_load_dwordx4 v[68:71], v[84:85], off offset:64
	global_load_dwordx4 v[64:67], v[160:161], off offset:64
	global_load_dwordx4 v[60:63], v[80:81], off offset:128
	global_load_dwordx4 v[56:59], v[82:83], off offset:128
	global_load_dwordx4 v[52:55], v[84:85], off offset:128
	global_load_dwordx4 v[48:51], v[160:161], off offset:128
	global_load_dwordx4 v[108:111], v[80:81], off offset:192
	global_load_dwordx4 v[104:107], v[82:83], off offset:192
	global_load_dwordx4 v[100:103], v[84:85], off offset:192
	global_load_dwordx4 v[96:99], v[160:161], off offset:192
	global_load_dwordx4 v[92:95], v[80:81], off offset:256
	global_load_dwordx4 v[88:91], v[82:83], off offset:256
	s_nop 0
	global_load_dwordx4 v[84:87], v[84:85], off offset:256
	s_nop 0
	global_load_dwordx4 v[80:83], v[160:161], off offset:256
	s_add_i32 s38, s38, s40
	s_waitcnt vmcnt(16)
	v_cvt_f32_f16_e32 v178, v44
	v_cvt_f32_f16_sdwa v179, v44 dst_sel:DWORD dst_unused:UNUSED_PAD src0_sel:WORD_1
	v_cvt_f32_f16_e32 v44, v45
	v_cvt_f32_f16_sdwa v45, v45 dst_sel:DWORD dst_unused:UNUSED_PAD src0_sel:WORD_1
	v_cvt_f32_f16_e32 v180, v46
	v_cvt_f32_f16_sdwa v181, v46 dst_sel:DWORD dst_unused:UNUSED_PAD src0_sel:WORD_1
	v_cvt_f32_f16_e32 v46, v47
	v_cvt_f32_f16_sdwa v47, v47 dst_sel:DWORD dst_unused:UNUSED_PAD src0_sel:WORD_1
	v_pk_mul_f32 v[206:207], v[178:179], v[178:179]
	v_pk_mul_f32 v[208:209], v[44:45], v[44:45]
	v_cvt_f32_f16_e32 v160, v32
	v_cvt_f32_f16_sdwa v161, v32 dst_sel:DWORD dst_unused:UNUSED_PAD src0_sel:WORD_1
	v_cvt_f32_f16_e32 v32, v33
	v_cvt_f32_f16_sdwa v33, v33 dst_sel:DWORD dst_unused:UNUSED_PAD src0_sel:WORD_1
	v_cvt_f32_f16_e32 v162, v34
	v_cvt_f32_f16_sdwa v163, v34 dst_sel:DWORD dst_unused:UNUSED_PAD src0_sel:WORD_1
	v_cvt_f32_f16_e32 v34, v35
	v_cvt_f32_f16_sdwa v35, v35 dst_sel:DWORD dst_unused:UNUSED_PAD src0_sel:WORD_1
	v_cvt_f32_f16_e32 v164, v36
	v_cvt_f32_f16_sdwa v165, v36 dst_sel:DWORD dst_unused:UNUSED_PAD src0_sel:WORD_1
	v_cvt_f32_f16_e32 v36, v37
	v_cvt_f32_f16_sdwa v37, v37 dst_sel:DWORD dst_unused:UNUSED_PAD src0_sel:WORD_1
	v_cvt_f32_f16_e32 v170, v38
	v_cvt_f32_f16_sdwa v171, v38 dst_sel:DWORD dst_unused:UNUSED_PAD src0_sel:WORD_1
	v_cvt_f32_f16_e32 v38, v39
	v_cvt_f32_f16_sdwa v39, v39 dst_sel:DWORD dst_unused:UNUSED_PAD src0_sel:WORD_1
	v_pk_mul_f32 v[182:183], v[160:161], v[160:161]
	v_pk_mul_f32 v[184:185], v[32:33], v[32:33]
	v_pk_mul_f32 v[186:187], v[162:163], v[162:163]
	v_pk_mul_f32 v[188:189], v[34:35], v[34:35]
	v_add_f32_e32 v186, v186, v187
	v_add_f32_e32 v175, v188, v189
	v_add_f32_e32 v184, v184, v185
	v_add_f32_e32 v182, v182, v183
	v_cvt_f32_f16_e32 v172, v40
	v_cvt_f32_f16_sdwa v173, v40 dst_sel:DWORD dst_unused:UNUSED_PAD src0_sel:WORD_1
	v_cvt_f32_f16_e32 v40, v41
	v_cvt_f32_f16_sdwa v41, v41 dst_sel:DWORD dst_unused:UNUSED_PAD src0_sel:WORD_1
	v_pk_mul_f32 v[190:191], v[164:165], v[164:165]
	v_pk_mul_f32 v[192:193], v[36:37], v[36:37]
	v_add_f32_e32 v175, v186, v175
	v_add_f32_e32 v182, v182, v184
	v_add_f32_e32 v175, v182, v175
	v_add_f32_e32 v182, v192, v193
	v_add_f32_e32 v183, v190, v191
	v_cvt_f32_f16_e32 v176, v42
	v_cvt_f32_f16_sdwa v177, v42 dst_sel:DWORD dst_unused:UNUSED_PAD src0_sel:WORD_1
	v_cvt_f32_f16_e32 v42, v43
	v_cvt_f32_f16_sdwa v43, v43 dst_sel:DWORD dst_unused:UNUSED_PAD src0_sel:WORD_1
	v_pk_mul_f32 v[194:195], v[170:171], v[170:171]
	v_pk_mul_f32 v[196:197], v[38:39], v[38:39]
	v_add_f32_e32 v182, v183, v182
	v_add_f32_e32 v175, v175, v182
	v_add_f32_e32 v182, v196, v197
	v_add_f32_e32 v183, v194, v195
	v_pk_mul_f32 v[198:199], v[172:173], v[172:173]
	v_pk_mul_f32 v[200:201], v[40:41], v[40:41]
	v_add_f32_e32 v182, v183, v182
	v_add_f32_e32 v175, v182, v175
	v_add_f32_e32 v182, v200, v201
	v_add_f32_e32 v183, v198, v199
	v_pk_mul_f32 v[202:203], v[176:177], v[176:177]
	v_pk_mul_f32 v[204:205], v[42:43], v[42:43]
	v_add_f32_e32 v182, v183, v182
	v_add_f32_e32 v175, v182, v175
	v_add_f32_e32 v182, v204, v205
	v_add_f32_e32 v183, v202, v203
	v_add_f32_e32 v182, v183, v182
	v_add_f32_e32 v175, v182, v175
	v_add_f32_e32 v182, v208, v209
	v_add_f32_e32 v183, v206, v207
	v_pk_mul_f32 v[210:211], v[180:181], v[180:181]
	v_pk_mul_f32 v[224:225], v[46:47], v[46:47]
	v_add_f32_e32 v182, v183, v182
	v_add_f32_e32 v175, v182, v175
	v_add_f32_e32 v182, v224, v225
	v_add_f32_e32 v183, v210, v211
	v_add_f32_e32 v182, v183, v182
	v_add_f32_e32 v175, v182, v175
	s_waitcnt vmcnt(12)
	v_cvt_f32_f16_e32 v186, v67
	v_cvt_f32_f16_sdwa v187, v67 dst_sel:DWORD dst_unused:UNUSED_PAD src0_sel:WORD_1
	v_add_f32_dpp v175, v175, v175 row_ror:8 row_mask:0xf bank_mask:0xf bound_ctrl:1
	v_pk_mul_f32 v[226:227], v[186:187], v[186:187]
	s_nop 0
	v_add_f32_dpp v175, v175, v175 row_ror:4 row_mask:0xf bank_mask:0xf bound_ctrl:1
	s_nop 1
	v_add_f32_dpp v175, v175, v175 row_ror:2 row_mask:0xf bank_mask:0xf bound_ctrl:1
	s_nop 1
	v_add_f32_dpp v175, v175, v175 row_ror:1 row_mask:0xf bank_mask:0xf bound_ctrl:1
	ds_swizzle_b32 v182, v175 offset:swizzle(SWAP,16)
	s_waitcnt lgkmcnt(0)
	v_add_f32_e32 v175, v175, v182
	s_nop 0
	v_readlane_b32 s1, v175, 32
	v_readlane_b32 s0, v175, 0
	s_nop 0
	v_mov_b32_e32 v175, s1
	v_add_f32_e32 v175, s0, v175
	v_fmamk_f32 v175, v175, 0x3a000000, v238
	v_rsq_f32_e32 v182, v175
	s_movk_i32 s0, 0x9000
	v_pk_mul_f32 v[160:161], v[160:161], v[182:183] op_sel_hi:[1,0]
	v_pk_mul_f32 v[32:33], v[32:33], v[182:183] op_sel_hi:[1,0]
	v_pk_mul_f32 v[34:35], v[34:35], v[182:183] op_sel_hi:[1,0]
	v_pk_fma_f32 v[184:185], v[128:129], v[32:33], v[6:7]
	v_pk_fma_f32 v[32:33], v[130:131], v[160:161], v[4:5]
	v_pk_mul_f32 v[160:161], v[162:163], v[182:183] op_sel_hi:[1,0]
	v_pk_fma_f32 v[162:163], v[132:133], v[34:35], v[2:3]
	v_pk_fma_f32 v[34:35], v[134:135], v[160:161], v[0:1]
	v_add_co_u32_e32 v160, vcc, s0, v126
	v_cvt_pk_bf16_f32 v32, v32, v33
	v_cvt_pk_bf16_f32 v33, v184, v185
	v_cvt_pk_bf16_f32 v34, v34, v35
	v_cvt_pk_bf16_f32 v35, v162, v163
	v_addc_co_u32_e32 v161, vcc, -1, v127, vcc
	global_store_dwordx4 v[160:161], v[32:35], off offset:-3072
	v_pk_mul_f32 v[38:39], v[38:39], v[182:183] op_sel_hi:[1,0]
	v_cvt_f32_f16_e32 v162, v76
	v_pk_mul_f32 v[32:33], v[164:165], v[182:183] op_sel_hi:[1,0]
	v_pk_mul_f32 v[34:35], v[36:37], v[182:183] op_sel_hi:[1,0]
	v_pk_mul_f32 v[36:37], v[170:171], v[182:183] op_sel_hi:[1,0]
	v_pk_fma_f32 v[34:35], v[136:137], v[34:35], v[14:15]
	v_pk_fma_f32 v[32:33], v[138:139], v[32:33], v[12:13]
	v_pk_fma_f32 v[38:39], v[140:141], v[38:39], v[10:11]
	v_pk_fma_f32 v[36:37], v[142:143], v[36:37], v[8:9]
	v_cvt_pk_bf16_f32 v32, v32, v33
	v_cvt_pk_bf16_f32 v33, v34, v35
	v_cvt_pk_bf16_f32 v34, v36, v37
	v_cvt_pk_bf16_f32 v35, v38, v39
	v_cvt_f32_f16_sdwa v163, v76 dst_sel:DWORD dst_unused:UNUSED_PAD src0_sel:WORD_1
	v_cvt_f32_f16_e32 v76, v77
	v_cvt_f32_f16_sdwa v77, v77 dst_sel:DWORD dst_unused:UNUSED_PAD src0_sel:WORD_1
	v_cvt_f32_f16_e32 v164, v78
	v_cvt_f32_f16_sdwa v165, v78 dst_sel:DWORD dst_unused:UNUSED_PAD src0_sel:WORD_1
	v_cvt_f32_f16_e32 v78, v79
	v_cvt_f32_f16_sdwa v79, v79 dst_sel:DWORD dst_unused:UNUSED_PAD src0_sel:WORD_1
	global_store_dwordx4 v[160:161], v[32:35], off offset:-2048
	v_pk_mul_f32 v[36:37], v[176:177], v[182:183] op_sel_hi:[1,0]
	v_pk_mul_f32 v[38:39], v[42:43], v[182:183] op_sel_hi:[1,0]
	v_pk_mul_f32 v[32:33], v[172:173], v[182:183] op_sel_hi:[1,0]
	v_pk_mul_f32 v[34:35], v[40:41], v[182:183] op_sel_hi:[1,0]
	v_cvt_f32_f16_e32 v170, v72
	v_cvt_f32_f16_sdwa v171, v72 dst_sel:DWORD dst_unused:UNUSED_PAD src0_sel:WORD_1
	v_cvt_f32_f16_e32 v72, v73
	v_cvt_f32_f16_sdwa v73, v73 dst_sel:DWORD dst_unused:UNUSED_PAD src0_sel:WORD_1
	v_pk_fma_f32 v[34:35], v[144:145], v[34:35], v[22:23]
	v_pk_fma_f32 v[32:33], v[146:147], v[32:33], v[20:21]
	v_pk_fma_f32 v[38:39], v[148:149], v[38:39], v[18:19]
	v_pk_fma_f32 v[36:37], v[150:151], v[36:37], v[16:17]
	v_cvt_pk_bf16_f32 v32, v32, v33
	v_cvt_pk_bf16_f32 v33, v34, v35
	v_cvt_pk_bf16_f32 v34, v36, v37
	v_cvt_pk_bf16_f32 v35, v38, v39
	v_cvt_f32_f16_e32 v172, v74
	v_cvt_f32_f16_sdwa v173, v74 dst_sel:DWORD dst_unused:UNUSED_PAD src0_sel:WORD_1
	v_cvt_f32_f16_e32 v74, v75
	v_cvt_f32_f16_sdwa v75, v75 dst_sel:DWORD dst_unused:UNUSED_PAD src0_sel:WORD_1
	global_store_dwordx4 v[160:161], v[32:35], off offset:-1024
	v_pk_mul_f32 v[36:37], v[180:181], v[182:183] op_sel_hi:[1,0]
	v_pk_mul_f32 v[38:39], v[46:47], v[182:183] op_sel_hi:[1,0]
	v_pk_mul_f32 v[32:33], v[178:179], v[182:183] op_sel_hi:[1,0]
	v_pk_mul_f32 v[34:35], v[44:45], v[182:183] op_sel_hi:[1,0]
	v_cvt_f32_f16_e32 v180, v64
	v_cvt_f32_f16_sdwa v181, v64 dst_sel:DWORD dst_unused:UNUSED_PAD src0_sel:WORD_1
	v_cvt_f32_f16_e32 v182, v65
	v_cvt_f32_f16_sdwa v183, v65 dst_sel:DWORD dst_unused:UNUSED_PAD src0_sel:WORD_1
	v_cvt_f32_f16_e32 v184, v66
	v_cvt_f32_f16_sdwa v185, v66 dst_sel:DWORD dst_unused:UNUSED_PAD src0_sel:WORD_1
	v_pk_mul_f32 v[64:65], v[162:163], v[162:163]
	v_pk_mul_f32 v[66:67], v[76:77], v[76:77]
	v_pk_mul_f32 v[188:189], v[164:165], v[164:165]
	v_pk_mul_f32 v[190:191], v[78:79], v[78:79]
	v_cvt_f32_f16_e32 v176, v68
	v_cvt_f32_f16_sdwa v177, v68 dst_sel:DWORD dst_unused:UNUSED_PAD src0_sel:WORD_1
	v_cvt_f32_f16_e32 v68, v69
	v_cvt_f32_f16_sdwa v69, v69 dst_sel:DWORD dst_unused:UNUSED_PAD src0_sel:WORD_1
	v_pk_mul_f32 v[192:193], v[170:171], v[170:171]
	v_pk_mul_f32 v[194:195], v[72:73], v[72:73]
	v_add_f32_e32 v175, v190, v191
	v_add_f32_e32 v188, v188, v189
	v_add_f32_e32 v66, v66, v67
	v_add_f32_e32 v64, v64, v65
	v_add_f32_e32 v175, v188, v175
	v_add_f32_e32 v64, v64, v66
	v_add_f32_e32 v65, v194, v195
	v_add_f32_e32 v66, v192, v193
	v_cvt_f32_f16_e32 v178, v70
	v_cvt_f32_f16_sdwa v179, v70 dst_sel:DWORD dst_unused:UNUSED_PAD src0_sel:WORD_1
	v_cvt_f32_f16_e32 v70, v71
	v_cvt_f32_f16_sdwa v71, v71 dst_sel:DWORD dst_unused:UNUSED_PAD src0_sel:WORD_1
	v_pk_mul_f32 v[196:197], v[172:173], v[172:173]
	v_pk_mul_f32 v[198:199], v[74:75], v[74:75]
	v_add_f32_e32 v64, v64, v175
	v_add_f32_e32 v65, v66, v65
	v_add_f32_e32 v64, v64, v65
	v_add_f32_e32 v65, v198, v199
	v_add_f32_e32 v66, v196, v197
	v_pk_mul_f32 v[200:201], v[176:177], v[176:177]
	v_pk_mul_f32 v[202:203], v[68:69], v[68:69]
	v_add_f32_e32 v65, v66, v65
	v_add_f32_e32 v64, v65, v64
	v_add_f32_e32 v65, v202, v203
	v_add_f32_e32 v66, v200, v201
	v_pk_mul_f32 v[204:205], v[178:179], v[178:179]
	v_pk_mul_f32 v[206:207], v[70:71], v[70:71]
	v_add_f32_e32 v65, v66, v65
	v_add_f32_e32 v64, v65, v64
	v_add_f32_e32 v65, v206, v207
	v_add_f32_e32 v66, v204, v205
	v_pk_mul_f32 v[208:209], v[180:181], v[180:181]
	v_pk_mul_f32 v[210:211], v[182:183], v[182:183]
	v_add_f32_e32 v65, v66, v65
	v_add_f32_e32 v64, v65, v64
	v_add_f32_e32 v65, v210, v211
	v_add_f32_e32 v66, v208, v209
	v_pk_mul_f32 v[224:225], v[184:185], v[184:185]
	v_add_f32_e32 v65, v66, v65
	v_add_f32_e32 v64, v65, v64
	v_add_f32_e32 v65, v226, v227
	v_add_f32_e32 v66, v224, v225
	v_add_f32_e32 v65, v66, v65
	v_add_f32_e32 v64, v65, v64
	s_movk_i32 s0, 0xa000
	v_pk_fma_f32 v[34:35], v[152:153], v[34:35], v[30:31]
	v_add_f32_dpp v64, v64, v64 row_ror:8 row_mask:0xf bank_mask:0xf bound_ctrl:1
	v_pk_fma_f32 v[32:33], v[154:155], v[32:33], v[28:29]
	v_pk_fma_f32 v[38:39], v[156:157], v[38:39], v[26:27]
	v_add_f32_dpp v64, v64, v64 row_ror:4 row_mask:0xf bank_mask:0xf bound_ctrl:1
	v_pk_fma_f32 v[36:37], v[158:159], v[36:37], v[24:25]
	v_add_co_u32_e32 v160, vcc, s0, v126
	v_add_f32_dpp v64, v64, v64 row_ror:2 row_mask:0xf bank_mask:0xf bound_ctrl:1
	s_add_i32 s0, s35, 32
	v_cvt_pk_bf16_f32 v32, v32, v33
	v_add_f32_dpp v64, v64, v64 row_ror:1 row_mask:0xf bank_mask:0xf bound_ctrl:1
	ds_swizzle_b32 v65, v64 offset:swizzle(SWAP,16)
	v_cvt_pk_bf16_f32 v33, v34, v35
	v_cvt_pk_bf16_f32 v34, v36, v37
	v_cvt_pk_bf16_f32 v35, v38, v39
	v_addc_co_u32_e32 v161, vcc, -1, v127, vcc
	s_waitcnt lgkmcnt(0)
	v_add_f32_e32 v64, v64, v65
	s_and_b32 s0, s0, 0x120
	v_readlane_b32 s1, v64, 32
	global_store_dwordx4 v[160:161], v[32:35], off offset:-4096
	s_nop 1
	v_or_b32_e32 v32, s0, v166
	v_readlane_b32 s0, v64, 0
	v_mov_b32_e32 v64, s1
	v_lshlrev_b32_e32 v212, 1, v32
	v_add_f32_e32 v64, s0, v64
	v_fmamk_f32 v64, v64, 0x3a000000, v238
	v_rsq_f32_e32 v188, v64
	v_lshl_add_u64 v[32:33], s[2:3], 0, v[212:213]
	v_lshl_add_u64 v[34:35], v[32:33], 0, v[118:119]
	global_load_dwordx4 v[44:47], v[34:35], off offset:256
	v_pk_mul_f32 v[64:65], v[162:163], v[188:189] op_sel_hi:[1,0]
	v_pk_mul_f32 v[66:67], v[76:77], v[188:189] op_sel_hi:[1,0]
	v_pk_mul_f32 v[76:77], v[164:165], v[188:189] op_sel_hi:[1,0]
	v_pk_mul_f32 v[78:79], v[78:79], v[188:189] op_sel_hi:[1,0]
	v_lshl_add_u64 v[34:35], v[32:33], 0, v[120:121]
	v_pk_fma_f32 v[66:67], v[128:129], v[66:67], v[6:7]
	v_pk_fma_f32 v[64:65], v[130:131], v[64:65], v[4:5]
	v_pk_fma_f32 v[78:79], v[132:133], v[78:79], v[2:3]
	v_pk_fma_f32 v[76:77], v[134:135], v[76:77], v[0:1]
	global_load_dwordx4 v[40:43], v[34:35], off offset:256
	v_lshl_add_u64 v[34:35], v[32:33], 0, v[122:123]
	v_lshl_add_u64 v[32:33], v[32:33], 0, v[124:125]
	v_cvt_pk_bf16_f32 v64, v64, v65
	v_cvt_pk_bf16_f32 v65, v66, v67
	v_cvt_pk_bf16_f32 v66, v76, v77
	v_cvt_pk_bf16_f32 v67, v78, v79
	global_load_dwordx4 v[36:39], v[34:35], off offset:256
	v_pk_mul_f32 v[74:75], v[74:75], v[188:189] op_sel_hi:[1,0]
	global_load_dwordx4 v[32:35], v[32:33], off offset:256
	v_pk_fma_f32 v[74:75], v[140:141], v[74:75], v[10:11]
	global_store_dwordx4 v[160:161], v[64:67], off offset:-3072
	v_pk_mul_f32 v[70:71], v[70:71], v[188:189] op_sel_hi:[1,0]
	s_waitcnt vmcnt(20)
	v_cvt_f32_f16_e32 v162, v62
	v_pk_mul_f32 v[64:65], v[170:171], v[188:189] op_sel_hi:[1,0]
	v_pk_mul_f32 v[66:67], v[72:73], v[188:189] op_sel_hi:[1,0]
	v_pk_mul_f32 v[72:73], v[172:173], v[188:189] op_sel_hi:[1,0]
	v_pk_fma_f32 v[66:67], v[136:137], v[66:67], v[14:15]
	v_pk_fma_f32 v[64:65], v[138:139], v[64:65], v[12:13]
	v_pk_fma_f32 v[72:73], v[142:143], v[72:73], v[8:9]
	v_cvt_pk_bf16_f32 v64, v64, v65
	v_cvt_pk_bf16_f32 v65, v66, v67
	v_cvt_pk_bf16_f32 v66, v72, v73
	v_cvt_pk_bf16_f32 v67, v74, v75
	global_store_dwordx4 v[160:161], v[64:67], off offset:-2048
	v_pk_fma_f32 v[70:71], v[148:149], v[70:71], v[18:19]
	v_cvt_f32_f16_sdwa v163, v62 dst_sel:DWORD dst_unused:UNUSED_PAD src0_sel:WORD_1
	v_pk_mul_f32 v[64:65], v[176:177], v[188:189] op_sel_hi:[1,0]
	v_pk_mul_f32 v[66:67], v[68:69], v[188:189] op_sel_hi:[1,0]
	v_pk_mul_f32 v[68:69], v[178:179], v[188:189] op_sel_hi:[1,0]
	v_pk_fma_f32 v[66:67], v[144:145], v[66:67], v[22:23]
	v_pk_fma_f32 v[64:65], v[146:147], v[64:65], v[20:21]
	v_pk_fma_f32 v[68:69], v[150:151], v[68:69], v[16:17]
	v_cvt_pk_bf16_f32 v64, v64, v65
	v_cvt_pk_bf16_f32 v65, v66, v67
	v_cvt_pk_bf16_f32 v66, v68, v69
	v_cvt_pk_bf16_f32 v67, v70, v71
	global_store_dwordx4 v[160:161], v[64:67], off offset:-1024
	v_pk_mul_f32 v[68:69], v[184:185], v[188:189] op_sel_hi:[1,0]
	v_pk_mul_f32 v[70:71], v[186:187], v[188:189] op_sel_hi:[1,0]
	v_pk_mul_f32 v[64:65], v[180:181], v[188:189] op_sel_hi:[1,0]
	v_pk_mul_f32 v[66:67], v[182:183], v[188:189] op_sel_hi:[1,0]
	v_pk_fma_f32 v[64:65], v[154:155], v[64:65], v[28:29]
	v_pk_fma_f32 v[66:67], v[152:153], v[66:67], v[30:31]
	v_pk_fma_f32 v[70:71], v[156:157], v[70:71], v[26:27]
	v_pk_fma_f32 v[68:69], v[158:159], v[68:69], v[24:25]
	v_cvt_pk_bf16_f32 v64, v64, v65
	v_cvt_pk_bf16_f32 v65, v66, v67
	v_cvt_pk_bf16_f32 v66, v68, v69
	v_cvt_pk_bf16_f32 v67, v70, v71
	global_store_dwordx4 v[160:161], v[64:67], off
	v_cvt_f32_f16_e32 v160, v60
	v_cvt_f32_f16_sdwa v161, v60 dst_sel:DWORD dst_unused:UNUSED_PAD src0_sel:WORD_1
	v_cvt_f32_f16_e32 v60, v61
	v_cvt_f32_f16_sdwa v61, v61 dst_sel:DWORD dst_unused:UNUSED_PAD src0_sel:WORD_1
	v_cvt_f32_f16_e32 v62, v63
	v_cvt_f32_f16_sdwa v63, v63 dst_sel:DWORD dst_unused:UNUSED_PAD src0_sel:WORD_1
	s_waitcnt vmcnt(22)
	v_cvt_f32_f16_e32 v164, v56
	v_cvt_f32_f16_sdwa v165, v56 dst_sel:DWORD dst_unused:UNUSED_PAD src0_sel:WORD_1
	v_cvt_f32_f16_e32 v56, v57
	v_cvt_f32_f16_sdwa v57, v57 dst_sel:DWORD dst_unused:UNUSED_PAD src0_sel:WORD_1
	v_cvt_f32_f16_e32 v170, v58
	v_cvt_f32_f16_sdwa v171, v58 dst_sel:DWORD dst_unused:UNUSED_PAD src0_sel:WORD_1
	v_cvt_f32_f16_e32 v58, v59
	v_cvt_f32_f16_sdwa v59, v59 dst_sel:DWORD dst_unused:UNUSED_PAD src0_sel:WORD_1
	s_waitcnt vmcnt(20)
	v_cvt_f32_f16_e32 v178, v48
	v_cvt_f32_f16_sdwa v179, v48 dst_sel:DWORD dst_unused:UNUSED_PAD src0_sel:WORD_1
	v_cvt_f32_f16_e32 v180, v49
	v_cvt_f32_f16_sdwa v181, v49 dst_sel:DWORD dst_unused:UNUSED_PAD src0_sel:WORD_1
	v_cvt_f32_f16_e32 v182, v50
	v_cvt_f32_f16_sdwa v183, v50 dst_sel:DWORD dst_unused:UNUSED_PAD src0_sel:WORD_1
	v_cvt_f32_f16_e32 v184, v51
	v_cvt_f32_f16_sdwa v185, v51 dst_sel:DWORD dst_unused:UNUSED_PAD src0_sel:WORD_1
	v_pk_mul_f32 v[48:49], v[160:161], v[160:161]
	v_pk_mul_f32 v[50:51], v[60:61], v[60:61]
	v_pk_mul_f32 v[186:187], v[162:163], v[162:163]
	v_pk_mul_f32 v[188:189], v[62:63], v[62:63]
	v_cvt_f32_f16_e32 v172, v52
	v_cvt_f32_f16_sdwa v173, v52 dst_sel:DWORD dst_unused:UNUSED_PAD src0_sel:WORD_1
	v_cvt_f32_f16_e32 v52, v53
	v_cvt_f32_f16_sdwa v53, v53 dst_sel:DWORD dst_unused:UNUSED_PAD src0_sel:WORD_1
	v_pk_mul_f32 v[190:191], v[164:165], v[164:165]
	v_pk_mul_f32 v[192:193], v[56:57], v[56:57]
	v_add_f32_e32 v175, v188, v189
	v_add_f32_e32 v186, v186, v187
	v_add_f32_e32 v50, v50, v51
	v_add_f32_e32 v48, v48, v49
	v_add_f32_e32 v175, v186, v175
	v_add_f32_e32 v48, v48, v50
	v_add_f32_e32 v49, v192, v193
	v_add_f32_e32 v50, v190, v191
	v_cvt_f32_f16_e32 v176, v54
	v_cvt_f32_f16_sdwa v177, v54 dst_sel:DWORD dst_unused:UNUSED_PAD src0_sel:WORD_1
	v_cvt_f32_f16_e32 v54, v55
	v_cvt_f32_f16_sdwa v55, v55 dst_sel:DWORD dst_unused:UNUSED_PAD src0_sel:WORD_1
	v_pk_mul_f32 v[194:195], v[170:171], v[170:171]
	v_pk_mul_f32 v[196:197], v[58:59], v[58:59]
	v_add_f32_e32 v48, v48, v175
	v_add_f32_e32 v49, v50, v49
	v_add_f32_e32 v48, v48, v49
	v_add_f32_e32 v49, v196, v197
	v_add_f32_e32 v50, v194, v195
	v_pk_mul_f32 v[198:199], v[172:173], v[172:173]
	v_pk_mul_f32 v[200:201], v[52:53], v[52:53]
	v_add_f32_e32 v49, v50, v49
	v_add_f32_e32 v48, v49, v48
	v_add_f32_e32 v49, v200, v201
	v_add_f32_e32 v50, v198, v199
	v_pk_mul_f32 v[202:203], v[176:177], v[176:177]
	v_pk_mul_f32 v[204:205], v[54:55], v[54:55]
	v_add_f32_e32 v49, v50, v49
	v_add_f32_e32 v48, v49, v48
	v_add_f32_e32 v49, v204, v205
	v_add_f32_e32 v50, v202, v203
	v_pk_mul_f32 v[206:207], v[178:179], v[178:179]
	v_pk_mul_f32 v[208:209], v[180:181], v[180:181]
	v_add_f32_e32 v49, v50, v49
	v_add_f32_e32 v48, v49, v48
	v_add_f32_e32 v49, v208, v209
	v_add_f32_e32 v50, v206, v207
	v_pk_mul_f32 v[210:211], v[182:183], v[182:183]
	v_pk_mul_f32 v[224:225], v[184:185], v[184:185]
	v_add_f32_e32 v49, v50, v49
	v_add_f32_e32 v48, v49, v48
	v_add_f32_e32 v49, v224, v225
	v_add_f32_e32 v50, v210, v211
	v_add_f32_e32 v49, v50, v49
	v_add_f32_e32 v48, v49, v48
	s_add_i32 s0, s35, 64
	s_and_b32 s0, s0, 0x140
	v_add_f32_dpp v48, v48, v48 row_ror:8 row_mask:0xf bank_mask:0xf bound_ctrl:1
	v_or_b32_e32 v64, s0, v166
	v_lshlrev_b32_e32 v212, 1, v64
	v_add_f32_dpp v48, v48, v48 row_ror:4 row_mask:0xf bank_mask:0xf bound_ctrl:1
	v_lshl_add_u64 v[64:65], s[2:3], 0, v[212:213]
	v_lshl_add_u64 v[66:67], v[64:65], 0, v[118:119]
	v_add_f32_dpp v48, v48, v48 row_ror:2 row_mask:0xf bank_mask:0xf bound_ctrl:1
	global_load_dwordx4 v[76:79], v[66:67], off offset:256
	v_lshl_add_u64 v[66:67], v[64:65], 0, v[120:121]
	v_add_f32_dpp v48, v48, v48 row_ror:1 row_mask:0xf bank_mask:0xf bound_ctrl:1
	ds_swizzle_b32 v49, v48 offset:swizzle(SWAP,16)
	global_load_dwordx4 v[72:75], v[66:67], off offset:256
	v_lshl_add_u64 v[66:67], v[64:65], 0, v[122:123]
	v_lshl_add_u64 v[64:65], v[64:65], 0, v[124:125]
	global_load_dwordx4 v[68:71], v[66:67], off offset:256
	s_waitcnt lgkmcnt(0)
	v_add_f32_e32 v48, v48, v49
	global_load_dwordx4 v[64:67], v[64:65], off offset:256
	v_readlane_b32 s1, v48, 32
	v_readlane_b32 s0, v48, 0
	s_nop 0
	v_mov_b32_e32 v48, s1
	v_add_f32_e32 v48, s0, v48
	v_fmamk_f32 v48, v48, 0x3a000000, v238
	v_rsq_f32_e32 v186, v48
	s_movk_i32 s0, 0xb000
	v_pk_mul_f32 v[48:49], v[160:161], v[186:187] op_sel_hi:[1,0]
	v_pk_mul_f32 v[50:51], v[60:61], v[186:187] op_sel_hi:[1,0]
	v_pk_mul_f32 v[60:61], v[162:163], v[186:187] op_sel_hi:[1,0]
	v_pk_fma_f32 v[50:51], v[128:129], v[50:51], v[6:7]
	v_pk_fma_f32 v[48:49], v[130:131], v[48:49], v[4:5]
	v_pk_mul_f32 v[62:63], v[62:63], v[186:187] op_sel_hi:[1,0]
	v_pk_fma_f32 v[60:61], v[134:135], v[60:61], v[0:1]
	v_pk_fma_f32 v[62:63], v[132:133], v[62:63], v[2:3]
	v_cvt_pk_bf16_f32 v48, v48, v49
	v_cvt_pk_bf16_f32 v49, v50, v51
	v_cvt_pk_bf16_f32 v50, v60, v61
	v_add_co_u32_e32 v60, vcc, s0, v126
	v_cvt_pk_bf16_f32 v51, v62, v63
	s_nop 0
	v_addc_co_u32_e32 v61, vcc, -1, v127, vcc
	global_store_dwordx4 v[60:61], v[48:51], off offset:-3072
	v_pk_mul_f32 v[58:59], v[58:59], v[186:187] op_sel_hi:[1,0]
	s_waitcnt vmcnt(24)
	v_cvt_f32_f16_e32 v162, v108
	v_pk_mul_f32 v[48:49], v[164:165], v[186:187] op_sel_hi:[1,0]
	v_pk_mul_f32 v[50:51], v[56:57], v[186:187] op_sel_hi:[1,0]
	v_pk_mul_f32 v[56:57], v[170:171], v[186:187] op_sel_hi:[1,0]
	v_pk_fma_f32 v[50:51], v[136:137], v[50:51], v[14:15]
	v_pk_fma_f32 v[48:49], v[138:139], v[48:49], v[12:13]
	v_pk_fma_f32 v[58:59], v[140:141], v[58:59], v[10:11]
	v_pk_fma_f32 v[56:57], v[142:143], v[56:57], v[8:9]
	v_cvt_pk_bf16_f32 v48, v48, v49
	v_cvt_pk_bf16_f32 v49, v50, v51
	v_cvt_pk_bf16_f32 v50, v56, v57
	v_cvt_pk_bf16_f32 v51, v58, v59
	v_cvt_f32_f16_sdwa v163, v108 dst_sel:DWORD dst_unused:UNUSED_PAD src0_sel:WORD_1
	v_cvt_f32_f16_e32 v108, v109
	v_cvt_f32_f16_sdwa v109, v109 dst_sel:DWORD dst_unused:UNUSED_PAD src0_sel:WORD_1
	v_cvt_f32_f16_e32 v164, v110
	v_cvt_f32_f16_sdwa v165, v110 dst_sel:DWORD dst_unused:UNUSED_PAD src0_sel:WORD_1
	v_cvt_f32_f16_e32 v110, v111
	v_cvt_f32_f16_sdwa v111, v111 dst_sel:DWORD dst_unused:UNUSED_PAD src0_sel:WORD_1
	global_store_dwordx4 v[60:61], v[48:51], off offset:-2048
	v_pk_mul_f32 v[54:55], v[54:55], v[186:187] op_sel_hi:[1,0]
	s_waitcnt vmcnt(24)
	v_cvt_f32_f16_e32 v170, v104
	v_pk_mul_f32 v[48:49], v[172:173], v[186:187] op_sel_hi:[1,0]
	v_pk_mul_f32 v[50:51], v[52:53], v[186:187] op_sel_hi:[1,0]
	v_pk_mul_f32 v[52:53], v[176:177], v[186:187] op_sel_hi:[1,0]
	v_cvt_f32_f16_sdwa v171, v104 dst_sel:DWORD dst_unused:UNUSED_PAD src0_sel:WORD_1
	v_cvt_f32_f16_e32 v104, v105
	v_cvt_f32_f16_sdwa v105, v105 dst_sel:DWORD dst_unused:UNUSED_PAD src0_sel:WORD_1
	v_pk_fma_f32 v[50:51], v[144:145], v[50:51], v[22:23]
	v_pk_fma_f32 v[48:49], v[146:147], v[48:49], v[20:21]
	v_pk_fma_f32 v[54:55], v[148:149], v[54:55], v[18:19]
	v_pk_fma_f32 v[52:53], v[150:151], v[52:53], v[16:17]
	v_cvt_pk_bf16_f32 v48, v48, v49
	v_cvt_pk_bf16_f32 v49, v50, v51
	v_cvt_pk_bf16_f32 v50, v52, v53
	v_cvt_pk_bf16_f32 v51, v54, v55
	v_cvt_f32_f16_e32 v172, v106
	v_cvt_f32_f16_sdwa v173, v106 dst_sel:DWORD dst_unused:UNUSED_PAD src0_sel:WORD_1
	v_cvt_f32_f16_e32 v106, v107
	v_cvt_f32_f16_sdwa v107, v107 dst_sel:DWORD dst_unused:UNUSED_PAD src0_sel:WORD_1
	global_store_dwordx4 v[60:61], v[48:51], off offset:-1024
	v_pk_mul_f32 v[52:53], v[182:183], v[186:187] op_sel_hi:[1,0]
	v_pk_mul_f32 v[54:55], v[184:185], v[186:187] op_sel_hi:[1,0]
	v_pk_mul_f32 v[48:49], v[178:179], v[186:187] op_sel_hi:[1,0]
	v_pk_mul_f32 v[50:51], v[180:181], v[186:187] op_sel_hi:[1,0]
	s_waitcnt vmcnt(23)
	v_cvt_f32_f16_e32 v180, v96
	v_cvt_f32_f16_sdwa v181, v96 dst_sel:DWORD dst_unused:UNUSED_PAD src0_sel:WORD_1
	v_cvt_f32_f16_e32 v182, v97
	v_cvt_f32_f16_sdwa v183, v97 dst_sel:DWORD dst_unused:UNUSED_PAD src0_sel:WORD_1
	v_cvt_f32_f16_e32 v184, v98
	v_cvt_f32_f16_sdwa v185, v98 dst_sel:DWORD dst_unused:UNUSED_PAD src0_sel:WORD_1
	v_cvt_f32_f16_e32 v186, v99
	v_cvt_f32_f16_sdwa v187, v99 dst_sel:DWORD dst_unused:UNUSED_PAD src0_sel:WORD_1
	v_pk_mul_f32 v[96:97], v[162:163], v[162:163]
	v_pk_mul_f32 v[98:99], v[108:109], v[108:109]
	v_pk_mul_f32 v[188:189], v[164:165], v[164:165]
	v_pk_mul_f32 v[190:191], v[110:111], v[110:111]
	v_cvt_f32_f16_e32 v176, v100
	v_cvt_f32_f16_sdwa v177, v100 dst_sel:DWORD dst_unused:UNUSED_PAD src0_sel:WORD_1
	v_cvt_f32_f16_e32 v100, v101
	v_cvt_f32_f16_sdwa v101, v101 dst_sel:DWORD dst_unused:UNUSED_PAD src0_sel:WORD_1
	v_pk_mul_f32 v[192:193], v[170:171], v[170:171]
	v_pk_mul_f32 v[194:195], v[104:105], v[104:105]
	v_add_f32_e32 v175, v190, v191
	v_add_f32_e32 v188, v188, v189
	v_add_f32_e32 v98, v98, v99
	v_add_f32_e32 v96, v96, v97
	v_add_f32_e32 v175, v188, v175
	v_add_f32_e32 v96, v96, v98
	v_add_f32_e32 v97, v194, v195
	v_add_f32_e32 v98, v192, v193
	v_cvt_f32_f16_e32 v178, v102
	v_cvt_f32_f16_sdwa v179, v102 dst_sel:DWORD dst_unused:UNUSED_PAD src0_sel:WORD_1
	v_cvt_f32_f16_e32 v102, v103
	v_cvt_f32_f16_sdwa v103, v103 dst_sel:DWORD dst_unused:UNUSED_PAD src0_sel:WORD_1
	v_pk_mul_f32 v[196:197], v[172:173], v[172:173]
	v_pk_mul_f32 v[198:199], v[106:107], v[106:107]
	v_add_f32_e32 v96, v96, v175
	v_add_f32_e32 v97, v98, v97
	v_add_f32_e32 v96, v96, v97
	v_add_f32_e32 v97, v198, v199
	v_add_f32_e32 v98, v196, v197
	v_pk_mul_f32 v[200:201], v[176:177], v[176:177]
	v_pk_mul_f32 v[202:203], v[100:101], v[100:101]
	v_add_f32_e32 v97, v98, v97
	v_add_f32_e32 v96, v97, v96
	v_add_f32_e32 v97, v202, v203
	v_add_f32_e32 v98, v200, v201
	v_pk_mul_f32 v[204:205], v[178:179], v[178:179]
	v_pk_mul_f32 v[206:207], v[102:103], v[102:103]
	v_add_f32_e32 v97, v98, v97
	v_add_f32_e32 v96, v97, v96
	v_add_f32_e32 v97, v206, v207
	v_add_f32_e32 v98, v204, v205
	v_pk_mul_f32 v[208:209], v[180:181], v[180:181]
	v_pk_mul_f32 v[210:211], v[182:183], v[182:183]
	v_add_f32_e32 v97, v98, v97
	v_add_f32_e32 v96, v97, v96
	v_add_f32_e32 v97, v210, v211
	v_add_f32_e32 v98, v208, v209
	v_pk_mul_f32 v[224:225], v[184:185], v[184:185]
	v_pk_mul_f32 v[226:227], v[186:187], v[186:187]
	v_add_f32_e32 v97, v98, v97
	v_add_f32_e32 v96, v97, v96
	v_add_f32_e32 v97, v226, v227
	v_add_f32_e32 v98, v224, v225
	v_add_f32_e32 v97, v98, v97
	v_add_f32_e32 v96, v97, v96
	s_movk_i32 s0, 0xc000
	v_pk_fma_f32 v[50:51], v[152:153], v[50:51], v[30:31]
	v_add_f32_dpp v96, v96, v96 row_ror:8 row_mask:0xf bank_mask:0xf bound_ctrl:1
	v_pk_fma_f32 v[48:49], v[154:155], v[48:49], v[28:29]
	v_pk_fma_f32 v[54:55], v[156:157], v[54:55], v[26:27]
	v_add_f32_dpp v96, v96, v96 row_ror:4 row_mask:0xf bank_mask:0xf bound_ctrl:1
	v_pk_fma_f32 v[52:53], v[158:159], v[52:53], v[24:25]
	v_add_co_u32_e32 v160, vcc, s0, v126
	v_add_f32_dpp v96, v96, v96 row_ror:2 row_mask:0xf bank_mask:0xf bound_ctrl:1
	s_add_i32 s0, s35, 0x60
	v_cvt_pk_bf16_f32 v48, v48, v49
	v_add_f32_dpp v96, v96, v96 row_ror:1 row_mask:0xf bank_mask:0xf bound_ctrl:1
	ds_swizzle_b32 v97, v96 offset:swizzle(SWAP,16)
	v_cvt_pk_bf16_f32 v49, v50, v51
	v_cvt_pk_bf16_f32 v50, v52, v53
	v_cvt_pk_bf16_f32 v51, v54, v55
	v_addc_co_u32_e32 v161, vcc, -1, v127, vcc
	s_waitcnt lgkmcnt(0)
	v_add_f32_e32 v96, v96, v97
	s_and_b32 s0, s0, 0x160
	v_readlane_b32 s1, v96, 32
	global_store_dwordx4 v[160:161], v[48:51], off offset:-4096
	s_add_i32 s35, s35, s39
	s_cmpk_lt_i32 s38, 0x4000
	v_or_b32_e32 v48, s0, v166
	v_readlane_b32 s0, v96, 0
	v_mov_b32_e32 v96, s1
	v_lshlrev_b32_e32 v212, 1, v48
	v_add_f32_e32 v96, s0, v96
	v_fmamk_f32 v96, v96, 0x3a000000, v238
	v_rsq_f32_e32 v188, v96
	v_lshl_add_u64 v[48:49], s[2:3], 0, v[212:213]
	v_lshl_add_u64 v[50:51], v[48:49], 0, v[118:119]
	global_load_dwordx4 v[60:63], v[50:51], off offset:256
	v_pk_mul_f32 v[96:97], v[162:163], v[188:189] op_sel_hi:[1,0]
	v_pk_mul_f32 v[98:99], v[108:109], v[188:189] op_sel_hi:[1,0]
	v_pk_mul_f32 v[108:109], v[164:165], v[188:189] op_sel_hi:[1,0]
	v_pk_mul_f32 v[110:111], v[110:111], v[188:189] op_sel_hi:[1,0]
	v_lshl_add_u64 v[50:51], v[48:49], 0, v[120:121]
	v_pk_fma_f32 v[98:99], v[128:129], v[98:99], v[6:7]
	v_pk_fma_f32 v[96:97], v[130:131], v[96:97], v[4:5]
	v_pk_fma_f32 v[110:111], v[132:133], v[110:111], v[2:3]
	v_pk_fma_f32 v[108:109], v[134:135], v[108:109], v[0:1]
	global_load_dwordx4 v[56:59], v[50:51], off offset:256
	v_lshl_add_u64 v[50:51], v[48:49], 0, v[122:123]
	v_lshl_add_u64 v[48:49], v[48:49], 0, v[124:125]
	v_cvt_pk_bf16_f32 v96, v96, v97
	v_cvt_pk_bf16_f32 v97, v98, v99
	v_cvt_pk_bf16_f32 v98, v108, v109
	v_cvt_pk_bf16_f32 v99, v110, v111
	global_load_dwordx4 v[52:55], v[50:51], off offset:256
	v_pk_mul_f32 v[106:107], v[106:107], v[188:189] op_sel_hi:[1,0]
	global_load_dwordx4 v[48:51], v[48:49], off offset:256
	v_pk_fma_f32 v[106:107], v[140:141], v[106:107], v[10:11]
	global_store_dwordx4 v[160:161], v[96:99], off offset:-3072
	v_pk_mul_f32 v[102:103], v[102:103], v[188:189] op_sel_hi:[1,0]
	s_waitcnt vmcnt(28)
	v_cvt_f32_f16_e32 v108, v94
	v_pk_mul_f32 v[96:97], v[170:171], v[188:189] op_sel_hi:[1,0]
	v_pk_mul_f32 v[98:99], v[104:105], v[188:189] op_sel_hi:[1,0]
	v_pk_mul_f32 v[104:105], v[172:173], v[188:189] op_sel_hi:[1,0]
	v_pk_fma_f32 v[98:99], v[136:137], v[98:99], v[14:15]
	v_pk_fma_f32 v[96:97], v[138:139], v[96:97], v[12:13]
	v_pk_fma_f32 v[104:105], v[142:143], v[104:105], v[8:9]
	v_cvt_pk_bf16_f32 v96, v96, v97
	v_cvt_pk_bf16_f32 v97, v98, v99
	v_cvt_pk_bf16_f32 v98, v104, v105
	v_cvt_pk_bf16_f32 v99, v106, v107
	global_store_dwordx4 v[160:161], v[96:99], off offset:-2048
	v_pk_fma_f32 v[102:103], v[148:149], v[102:103], v[18:19]
	v_cvt_f32_f16_e32 v104, v92
	v_pk_mul_f32 v[96:97], v[176:177], v[188:189] op_sel_hi:[1,0]
	v_pk_mul_f32 v[98:99], v[100:101], v[188:189] op_sel_hi:[1,0]
	v_pk_mul_f32 v[100:101], v[178:179], v[188:189] op_sel_hi:[1,0]
	v_pk_fma_f32 v[98:99], v[144:145], v[98:99], v[22:23]
	v_pk_fma_f32 v[96:97], v[146:147], v[96:97], v[20:21]
	v_pk_fma_f32 v[100:101], v[150:151], v[100:101], v[16:17]
	v_cvt_pk_bf16_f32 v96, v96, v97
	v_cvt_pk_bf16_f32 v97, v98, v99
	v_cvt_pk_bf16_f32 v98, v100, v101
	v_cvt_pk_bf16_f32 v99, v102, v103
	global_store_dwordx4 v[160:161], v[96:99], off offset:-1024
	v_pk_mul_f32 v[100:101], v[184:185], v[188:189] op_sel_hi:[1,0]
	v_pk_mul_f32 v[102:103], v[186:187], v[188:189] op_sel_hi:[1,0]
	v_pk_mul_f32 v[96:97], v[180:181], v[188:189] op_sel_hi:[1,0]
	v_pk_mul_f32 v[98:99], v[182:183], v[188:189] op_sel_hi:[1,0]
	v_cvt_f32_f16_sdwa v105, v92 dst_sel:DWORD dst_unused:UNUSED_PAD src0_sel:WORD_1
	v_cvt_f32_f16_e32 v106, v93
	v_cvt_f32_f16_sdwa v107, v93 dst_sel:DWORD dst_unused:UNUSED_PAD src0_sel:WORD_1
	v_cvt_f32_f16_sdwa v109, v94 dst_sel:DWORD dst_unused:UNUSED_PAD src0_sel:WORD_1
	v_cvt_f32_f16_e32 v110, v95
	v_cvt_f32_f16_sdwa v111, v95 dst_sel:DWORD dst_unused:UNUSED_PAD src0_sel:WORD_1
	v_pk_fma_f32 v[98:99], v[152:153], v[98:99], v[30:31]
	v_pk_fma_f32 v[96:97], v[154:155], v[96:97], v[28:29]
	v_pk_fma_f32 v[102:103], v[156:157], v[102:103], v[26:27]
	v_pk_fma_f32 v[100:101], v[158:159], v[100:101], v[24:25]
	s_waitcnt vmcnt(29)
	v_cvt_f32_f16_e32 v92, v88
	v_cvt_f32_f16_sdwa v93, v88 dst_sel:DWORD dst_unused:UNUSED_PAD src0_sel:WORD_1
	v_cvt_f32_f16_e32 v94, v89
	v_cvt_f32_f16_sdwa v95, v89 dst_sel:DWORD dst_unused:UNUSED_PAD src0_sel:WORD_1
	v_cvt_pk_bf16_f32 v96, v96, v97
	v_cvt_pk_bf16_f32 v97, v98, v99
	v_cvt_pk_bf16_f32 v98, v100, v101
	v_cvt_pk_bf16_f32 v99, v102, v103
	global_store_dwordx4 v[160:161], v[96:99], off
	v_cvt_f32_f16_e32 v100, v91
	v_cvt_f32_f16_sdwa v101, v91 dst_sel:DWORD dst_unused:UNUSED_PAD src0_sel:WORD_1
	v_cvt_f32_f16_e32 v96, v90
	v_cvt_f32_f16_sdwa v97, v90 dst_sel:DWORD dst_unused:UNUSED_PAD src0_sel:WORD_1
	v_pk_mul_f32 v[160:161], v[104:105], v[104:105]
	v_pk_mul_f32 v[162:163], v[106:107], v[106:107]
	v_pk_mul_f32 v[164:165], v[108:109], v[108:109]
	v_pk_mul_f32 v[170:171], v[110:111], v[110:111]
	s_waitcnt vmcnt(29)
	v_cvt_f32_f16_e32 v88, v84
	v_cvt_f32_f16_sdwa v89, v84 dst_sel:DWORD dst_unused:UNUSED_PAD src0_sel:WORD_1
	v_cvt_f32_f16_e32 v90, v85
	v_cvt_f32_f16_sdwa v91, v85 dst_sel:DWORD dst_unused:UNUSED_PAD src0_sel:WORD_1
	v_pk_mul_f32 v[172:173], v[92:93], v[92:93]
	v_pk_mul_f32 v[176:177], v[94:95], v[94:95]
	v_add_f32_e32 v170, v170, v171
	v_add_f32_e32 v164, v164, v165
	v_add_f32_e32 v162, v162, v163
	v_add_f32_e32 v160, v160, v161
	v_add_f32_e32 v164, v164, v170
	v_add_f32_e32 v160, v160, v162
	v_add_f32_e32 v161, v176, v177
	v_add_f32_e32 v162, v172, v173
	v_cvt_f32_f16_e32 v98, v86
	v_cvt_f32_f16_sdwa v99, v86 dst_sel:DWORD dst_unused:UNUSED_PAD src0_sel:WORD_1
	v_cvt_f32_f16_e32 v102, v87
	v_cvt_f32_f16_sdwa v103, v87 dst_sel:DWORD dst_unused:UNUSED_PAD src0_sel:WORD_1
	v_pk_mul_f32 v[178:179], v[96:97], v[96:97]
	v_pk_mul_f32 v[180:181], v[100:101], v[100:101]
	v_add_f32_e32 v160, v160, v164
	v_add_f32_e32 v161, v162, v161
	v_add_f32_e32 v160, v160, v161
	v_add_f32_e32 v161, v180, v181
	v_add_f32_e32 v162, v178, v179
	s_waitcnt vmcnt(28)
	v_cvt_f32_f16_e32 v84, v80
	v_cvt_f32_f16_sdwa v85, v80 dst_sel:DWORD dst_unused:UNUSED_PAD src0_sel:WORD_1
	v_cvt_f32_f16_e32 v80, v81
	v_cvt_f32_f16_sdwa v81, v81 dst_sel:DWORD dst_unused:UNUSED_PAD src0_sel:WORD_1
	v_pk_mul_f32 v[182:183], v[88:89], v[88:89]
	v_pk_mul_f32 v[184:185], v[90:91], v[90:91]
	v_add_f32_e32 v161, v162, v161
	v_add_f32_e32 v160, v161, v160
	v_add_f32_e32 v161, v184, v185
	v_add_f32_e32 v162, v182, v183
	v_cvt_f32_f16_e32 v86, v82
	v_cvt_f32_f16_sdwa v87, v82 dst_sel:DWORD dst_unused:UNUSED_PAD src0_sel:WORD_1
	v_cvt_f32_f16_e32 v82, v83
	v_cvt_f32_f16_sdwa v83, v83 dst_sel:DWORD dst_unused:UNUSED_PAD src0_sel:WORD_1
	v_pk_mul_f32 v[186:187], v[98:99], v[98:99]
	v_pk_mul_f32 v[188:189], v[102:103], v[102:103]
	v_add_f32_e32 v161, v162, v161
	v_add_f32_e32 v160, v161, v160
	v_add_f32_e32 v161, v188, v189
	v_add_f32_e32 v162, v186, v187
	v_pk_mul_f32 v[190:191], v[84:85], v[84:85]
	v_pk_mul_f32 v[192:193], v[80:81], v[80:81]
	v_add_f32_e32 v161, v162, v161
	v_add_f32_e32 v160, v161, v160
	v_add_f32_e32 v161, v192, v193
	v_add_f32_e32 v162, v190, v191
	v_pk_mul_f32 v[194:195], v[86:87], v[86:87]
	v_pk_mul_f32 v[196:197], v[82:83], v[82:83]
	v_add_f32_e32 v161, v162, v161
	v_add_f32_e32 v160, v161, v160
	v_add_f32_e32 v161, v196, v197
	v_add_f32_e32 v162, v194, v195
	v_add_f32_e32 v161, v162, v161
	v_add_f32_e32 v160, v161, v160
	s_nop 1
	v_add_f32_dpp v160, v160, v160 row_ror:8 row_mask:0xf bank_mask:0xf bound_ctrl:1
	s_nop 1
	v_add_f32_dpp v160, v160, v160 row_ror:4 row_mask:0xf bank_mask:0xf bound_ctrl:1
	s_nop 1
	v_add_f32_dpp v160, v160, v160 row_ror:2 row_mask:0xf bank_mask:0xf bound_ctrl:1
	s_nop 1
	v_add_f32_dpp v160, v160, v160 row_ror:1 row_mask:0xf bank_mask:0xf bound_ctrl:1
	ds_swizzle_b32 v161, v160 offset:swizzle(SWAP,16)
	s_waitcnt lgkmcnt(0)
	v_add_f32_e32 v160, v160, v161
	s_nop 0
	v_readlane_b32 s1, v160, 32
	v_readlane_b32 s0, v160, 0
	s_nop 0
	v_mov_b32_e32 v160, s1
	v_add_f32_e32 v160, s0, v160
	v_fmamk_f32 v160, v160, 0x3a000000, v238
	v_rsq_f32_e32 v160, v160
	s_movk_i32 s0, 0xd000
	v_pk_mul_f32 v[104:105], v[104:105], v[160:161] op_sel_hi:[1,0]
	v_pk_mul_f32 v[106:107], v[106:107], v[160:161] op_sel_hi:[1,0]
	v_pk_mul_f32 v[108:109], v[108:109], v[160:161] op_sel_hi:[1,0]
	v_pk_fma_f32 v[106:107], v[128:129], v[106:107], v[6:7]
	v_pk_fma_f32 v[104:105], v[130:131], v[104:105], v[4:5]
	v_pk_fma_f32 v[108:109], v[134:135], v[108:109], v[0:1]
	v_pk_mul_f32 v[92:93], v[92:93], v[160:161] op_sel_hi:[1,0]
	v_pk_mul_f32 v[94:95], v[94:95], v[160:161] op_sel_hi:[1,0]
	v_pk_mul_f32 v[96:97], v[96:97], v[160:161] op_sel_hi:[1,0]
	v_pk_mul_f32 v[100:101], v[100:101], v[160:161] op_sel_hi:[1,0]
	v_cvt_pk_bf16_f32 v104, v104, v105
	v_cvt_pk_bf16_f32 v105, v106, v107
	v_cvt_pk_bf16_f32 v106, v108, v109
	v_add_co_u32_e32 v108, vcc, s0, v126
	v_pk_fma_f32 v[94:95], v[136:137], v[94:95], v[14:15]
	v_pk_fma_f32 v[92:93], v[138:139], v[92:93], v[12:13]
	v_pk_fma_f32 v[100:101], v[140:141], v[100:101], v[10:11]
	v_pk_fma_f32 v[96:97], v[142:143], v[96:97], v[8:9]
	v_addc_co_u32_e32 v109, vcc, -1, v127, vcc
	v_cvt_pk_bf16_f32 v92, v92, v93
	v_cvt_pk_bf16_f32 v93, v94, v95
	v_cvt_pk_bf16_f32 v94, v96, v97
	v_cvt_pk_bf16_f32 v95, v100, v101
	global_store_dwordx4 v[108:109], v[92:95], off offset:-2048
	v_pk_mul_f32 v[88:89], v[88:89], v[160:161] op_sel_hi:[1,0]
	v_pk_mul_f32 v[90:91], v[90:91], v[160:161] op_sel_hi:[1,0]
	v_pk_mul_f32 v[92:93], v[98:99], v[160:161] op_sel_hi:[1,0]
	v_pk_mul_f32 v[94:95], v[102:103], v[160:161] op_sel_hi:[1,0]
	v_pk_fma_f32 v[90:91], v[144:145], v[90:91], v[22:23]
	v_pk_fma_f32 v[88:89], v[146:147], v[88:89], v[20:21]
	v_pk_fma_f32 v[94:95], v[148:149], v[94:95], v[18:19]
	v_pk_fma_f32 v[92:93], v[150:151], v[92:93], v[16:17]
	v_cvt_pk_bf16_f32 v88, v88, v89
	v_cvt_pk_bf16_f32 v89, v90, v91
	v_cvt_pk_bf16_f32 v90, v92, v93
	v_cvt_pk_bf16_f32 v91, v94, v95
	v_pk_mul_f32 v[84:85], v[84:85], v[160:161] op_sel_hi:[1,0]
	v_pk_mul_f32 v[80:81], v[80:81], v[160:161] op_sel_hi:[1,0]
	global_store_dwordx4 v[108:109], v[88:91], off offset:-1024
	v_pk_mul_f32 v[82:83], v[82:83], v[160:161] op_sel_hi:[1,0]
	s_movk_i32 s0, 0xe000
	v_pk_fma_f32 v[88:89], v[152:153], v[80:81], v[30:31]
	v_pk_fma_f32 v[80:81], v[154:155], v[84:85], v[28:29]
	v_pk_mul_f32 v[84:85], v[86:87], v[160:161] op_sel_hi:[1,0]
	v_pk_fma_f32 v[86:87], v[156:157], v[82:83], v[26:27]
	v_pk_fma_f32 v[82:83], v[158:159], v[84:85], v[24:25]
	v_add_co_u32_e32 v84, vcc, s0, v126
	v_cvt_pk_bf16_f32 v80, v80, v81
	v_cvt_pk_bf16_f32 v81, v88, v89
	v_cvt_pk_bf16_f32 v82, v82, v83
	v_cvt_pk_bf16_f32 v83, v86, v87
	v_addc_co_u32_e32 v85, vcc, -1, v127, vcc
	global_store_dwordx4 v[84:85], v[80:83], off offset:-4096
	v_pk_mul_f32 v[110:111], v[110:111], v[160:161] op_sel_hi:[1,0]
	s_waitcnt vmcnt(25)
	v_cvt_f32_f16_e32 v86, v40
	v_cvt_f32_f16_e32 v80, v44
	v_cvt_f32_f16_sdwa v81, v44 dst_sel:DWORD dst_unused:UNUSED_PAD src0_sel:WORD_1
	v_cvt_f32_f16_e32 v44, v45
	v_cvt_f32_f16_sdwa v45, v45 dst_sel:DWORD dst_unused:UNUSED_PAD src0_sel:WORD_1
	v_cvt_f32_f16_e32 v82, v46
	v_cvt_f32_f16_sdwa v83, v46 dst_sel:DWORD dst_unused:UNUSED_PAD src0_sel:WORD_1
	v_cvt_f32_f16_e32 v46, v47
	v_cvt_f32_f16_sdwa v47, v47 dst_sel:DWORD dst_unused:UNUSED_PAD src0_sel:WORD_1
	v_cvt_f32_f16_sdwa v87, v40 dst_sel:DWORD dst_unused:UNUSED_PAD src0_sel:WORD_1
	v_cvt_f32_f16_e32 v40, v41
	v_cvt_f32_f16_sdwa v41, v41 dst_sel:DWORD dst_unused:UNUSED_PAD src0_sel:WORD_1
	v_pk_fma_f32 v[110:111], v[132:133], v[110:111], v[2:3]
	v_cvt_f32_f16_e32 v88, v42
	v_cvt_pk_bf16_f32 v107, v110, v111
	v_cvt_f32_f16_sdwa v89, v42 dst_sel:DWORD dst_unused:UNUSED_PAD src0_sel:WORD_1
	v_cvt_f32_f16_e32 v42, v43
	v_cvt_f32_f16_sdwa v43, v43 dst_sel:DWORD dst_unused:UNUSED_PAD src0_sel:WORD_1
	global_store_dwordx4 v[108:109], v[104:107], off offset:-3072
	s_waitcnt vmcnt(24)
	v_cvt_f32_f16_e32 v94, v32
	v_cvt_f32_f16_sdwa v95, v32 dst_sel:DWORD dst_unused:UNUSED_PAD src0_sel:WORD_1
	v_cvt_f32_f16_e32 v96, v33
	v_cvt_f32_f16_sdwa v97, v33 dst_sel:DWORD dst_unused:UNUSED_PAD src0_sel:WORD_1
	v_cvt_f32_f16_e32 v98, v34
	v_cvt_f32_f16_sdwa v99, v34 dst_sel:DWORD dst_unused:UNUSED_PAD src0_sel:WORD_1
	v_cvt_f32_f16_e32 v100, v35
	v_cvt_f32_f16_sdwa v101, v35 dst_sel:DWORD dst_unused:UNUSED_PAD src0_sel:WORD_1
	v_pk_mul_f32 v[32:33], v[80:81], v[80:81]
	v_pk_mul_f32 v[34:35], v[44:45], v[44:45]
	v_pk_mul_f32 v[102:103], v[82:83], v[82:83]
	v_pk_mul_f32 v[104:105], v[46:47], v[46:47]
	v_cvt_f32_f16_e32 v90, v36
	v_cvt_f32_f16_sdwa v91, v36 dst_sel:DWORD dst_unused:UNUSED_PAD src0_sel:WORD_1
	v_cvt_f32_f16_e32 v36, v37
	v_cvt_f32_f16_sdwa v37, v37 dst_sel:DWORD dst_unused:UNUSED_PAD src0_sel:WORD_1
	v_pk_mul_f32 v[106:107], v[86:87], v[86:87]
	v_pk_mul_f32 v[108:109], v[40:41], v[40:41]
	v_add_f32_e32 v104, v104, v105
	v_add_f32_e32 v102, v102, v103
	v_add_f32_e32 v34, v34, v35
	v_add_f32_e32 v32, v32, v33
	v_add_f32_e32 v102, v102, v104
	v_add_f32_e32 v32, v32, v34
	v_add_f32_e32 v33, v108, v109
	v_add_f32_e32 v34, v106, v107
	v_cvt_f32_f16_e32 v92, v38
	v_cvt_f32_f16_sdwa v93, v38 dst_sel:DWORD dst_unused:UNUSED_PAD src0_sel:WORD_1
	v_cvt_f32_f16_e32 v38, v39
	v_cvt_f32_f16_sdwa v39, v39 dst_sel:DWORD dst_unused:UNUSED_PAD src0_sel:WORD_1
	v_pk_mul_f32 v[110:111], v[88:89], v[88:89]
	v_pk_mul_f32 v[160:161], v[42:43], v[42:43]
	v_add_f32_e32 v32, v32, v102
	v_add_f32_e32 v33, v34, v33
	v_add_f32_e32 v32, v32, v33
	v_add_f32_e32 v33, v160, v161
	v_add_f32_e32 v34, v110, v111
	v_pk_mul_f32 v[162:163], v[90:91], v[90:91]
	v_pk_mul_f32 v[164:165], v[36:37], v[36:37]
	v_add_f32_e32 v33, v34, v33
	v_add_f32_e32 v32, v33, v32
	v_add_f32_e32 v33, v164, v165
	v_add_f32_e32 v34, v162, v163
	v_pk_mul_f32 v[170:171], v[92:93], v[92:93]
	v_pk_mul_f32 v[172:173], v[38:39], v[38:39]
	v_add_f32_e32 v33, v34, v33
	v_add_f32_e32 v32, v33, v32
	v_add_f32_e32 v33, v172, v173
	v_add_f32_e32 v34, v170, v171
	v_pk_mul_f32 v[176:177], v[94:95], v[94:95]
	v_pk_mul_f32 v[178:179], v[96:97], v[96:97]
	v_add_f32_e32 v33, v34, v33
	v_add_f32_e32 v32, v33, v32
	v_add_f32_e32 v33, v178, v179
	v_add_f32_e32 v34, v176, v177
	v_pk_mul_f32 v[180:181], v[98:99], v[98:99]
	v_pk_mul_f32 v[182:183], v[100:101], v[100:101]
	v_add_f32_e32 v33, v34, v33
	v_add_f32_e32 v32, v33, v32
	v_add_f32_e32 v33, v182, v183
	v_add_f32_e32 v34, v180, v181
	v_add_f32_e32 v33, v34, v33
	v_add_f32_e32 v32, v33, v32
	s_nop 1
	v_add_f32_dpp v32, v32, v32 row_ror:8 row_mask:0xf bank_mask:0xf bound_ctrl:1
	s_nop 1
	v_add_f32_dpp v32, v32, v32 row_ror:4 row_mask:0xf bank_mask:0xf bound_ctrl:1
	s_nop 1
	v_add_f32_dpp v32, v32, v32 row_ror:2 row_mask:0xf bank_mask:0xf bound_ctrl:1
	s_nop 1
	v_add_f32_dpp v32, v32, v32 row_ror:1 row_mask:0xf bank_mask:0xf bound_ctrl:1
	ds_swizzle_b32 v33, v32 offset:swizzle(SWAP,16)
	s_waitcnt lgkmcnt(0)
	v_add_f32_e32 v32, v32, v33
	s_nop 0
	v_readlane_b32 s1, v32, 32
	v_readlane_b32 s0, v32, 0
	s_nop 0
	v_mov_b32_e32 v32, s1
	v_add_f32_e32 v32, s0, v32
	v_fmamk_f32 v32, v32, 0x3a000000, v238
	v_rsq_f32_e32 v102, v32
	s_nop 0
	v_pk_mul_f32 v[32:33], v[80:81], v[102:103] op_sel_hi:[1,0]
	v_pk_mul_f32 v[34:35], v[44:45], v[102:103] op_sel_hi:[1,0]
	v_pk_mul_f32 v[44:45], v[82:83], v[102:103] op_sel_hi:[1,0]
	v_pk_mul_f32 v[46:47], v[46:47], v[102:103] op_sel_hi:[1,0]
	v_pk_fma_f32 v[34:35], v[128:129], v[34:35], v[6:7]
	v_pk_fma_f32 v[32:33], v[130:131], v[32:33], v[4:5]
	v_pk_fma_f32 v[46:47], v[132:133], v[46:47], v[2:3]
	v_pk_fma_f32 v[44:45], v[134:135], v[44:45], v[0:1]
	v_cvt_pk_bf16_f32 v32, v32, v33
	v_cvt_pk_bf16_f32 v33, v34, v35
	v_cvt_pk_bf16_f32 v34, v44, v45
	v_cvt_pk_bf16_f32 v35, v46, v47
	global_store_dwordx4 v[84:85], v[32:35], off offset:-3072
	v_pk_mul_f32 v[42:43], v[42:43], v[102:103] op_sel_hi:[1,0]
	v_pk_mul_f32 v[38:39], v[38:39], v[102:103] op_sel_hi:[1,0]
	v_pk_mul_f32 v[32:33], v[86:87], v[102:103] op_sel_hi:[1,0]
	v_pk_mul_f32 v[34:35], v[40:41], v[102:103] op_sel_hi:[1,0]
	v_pk_mul_f32 v[40:41], v[88:89], v[102:103] op_sel_hi:[1,0]
	v_pk_fma_f32 v[34:35], v[136:137], v[34:35], v[14:15]
	v_pk_fma_f32 v[32:33], v[138:139], v[32:33], v[12:13]
	v_pk_fma_f32 v[42:43], v[140:141], v[42:43], v[10:11]
	v_pk_fma_f32 v[40:41], v[142:143], v[40:41], v[8:9]
	v_cvt_pk_bf16_f32 v32, v32, v33
	v_cvt_pk_bf16_f32 v33, v34, v35
	v_cvt_pk_bf16_f32 v34, v40, v41
	v_cvt_pk_bf16_f32 v35, v42, v43
	global_store_dwordx4 v[84:85], v[32:35], off offset:-2048
	v_pk_fma_f32 v[38:39], v[148:149], v[38:39], v[18:19]
	s_waitcnt vmcnt(21)
	v_cvt_f32_f16_e32 v82, v78
	v_pk_mul_f32 v[32:33], v[90:91], v[102:103] op_sel_hi:[1,0]
	v_pk_mul_f32 v[34:35], v[36:37], v[102:103] op_sel_hi:[1,0]
	v_pk_mul_f32 v[36:37], v[92:93], v[102:103] op_sel_hi:[1,0]
	v_pk_fma_f32 v[34:35], v[144:145], v[34:35], v[22:23]
	v_pk_fma_f32 v[32:33], v[146:147], v[32:33], v[20:21]
	v_pk_fma_f32 v[36:37], v[150:151], v[36:37], v[16:17]
	v_cvt_pk_bf16_f32 v32, v32, v33
	v_cvt_pk_bf16_f32 v33, v34, v35
	v_cvt_pk_bf16_f32 v34, v36, v37
	v_cvt_pk_bf16_f32 v35, v38, v39
	global_store_dwordx4 v[84:85], v[32:35], off offset:-1024
	v_pk_mul_f32 v[36:37], v[98:99], v[102:103] op_sel_hi:[1,0]
	v_pk_mul_f32 v[38:39], v[100:101], v[102:103] op_sel_hi:[1,0]
	v_pk_mul_f32 v[32:33], v[94:95], v[102:103] op_sel_hi:[1,0]
	v_pk_mul_f32 v[34:35], v[96:97], v[102:103] op_sel_hi:[1,0]
	v_pk_fma_f32 v[32:33], v[154:155], v[32:33], v[28:29]
	v_pk_fma_f32 v[34:35], v[152:153], v[34:35], v[30:31]
	v_pk_fma_f32 v[38:39], v[156:157], v[38:39], v[26:27]
	v_pk_fma_f32 v[36:37], v[158:159], v[36:37], v[24:25]
	v_cvt_pk_bf16_f32 v32, v32, v33
	v_cvt_pk_bf16_f32 v33, v34, v35
	v_cvt_pk_bf16_f32 v34, v36, v37
	v_cvt_pk_bf16_f32 v35, v38, v39
	global_store_dwordx4 v[84:85], v[32:35], off
	v_cvt_f32_f16_sdwa v83, v78 dst_sel:DWORD dst_unused:UNUSED_PAD src0_sel:WORD_1
	v_cvt_f32_f16_e32 v84, v79
	v_cvt_f32_f16_e32 v32, v76
	v_cvt_f32_f16_sdwa v33, v76 dst_sel:DWORD dst_unused:UNUSED_PAD src0_sel:WORD_1
	v_cvt_f32_f16_e32 v34, v77
	v_cvt_f32_f16_sdwa v35, v77 dst_sel:DWORD dst_unused:UNUSED_PAD src0_sel:WORD_1
	v_cvt_f32_f16_sdwa v85, v79 dst_sel:DWORD dst_unused:UNUSED_PAD src0_sel:WORD_1
	s_waitcnt vmcnt(22)
	v_cvt_f32_f16_e32 v78, v72
	v_cvt_f32_f16_sdwa v79, v72 dst_sel:DWORD dst_unused:UNUSED_PAD src0_sel:WORD_1
	v_cvt_f32_f16_e32 v80, v73
	v_cvt_f32_f16_sdwa v81, v73 dst_sel:DWORD dst_unused:UNUSED_PAD src0_sel:WORD_1
	v_cvt_f32_f16_e32 v76, v74
	v_cvt_f32_f16_sdwa v77, v74 dst_sel:DWORD dst_unused:UNUSED_PAD src0_sel:WORD_1
	v_cvt_f32_f16_e32 v74, v75
	v_cvt_f32_f16_sdwa v75, v75 dst_sel:DWORD dst_unused:UNUSED_PAD src0_sel:WORD_1
	s_waitcnt vmcnt(21)
	v_cvt_f32_f16_e32 v46, v68
	v_cvt_f32_f16_sdwa v47, v68 dst_sel:DWORD dst_unused:UNUSED_PAD src0_sel:WORD_1
	v_cvt_f32_f16_e32 v72, v69
	v_cvt_f32_f16_sdwa v73, v69 dst_sel:DWORD dst_unused:UNUSED_PAD src0_sel:WORD_1
	v_cvt_f32_f16_e32 v44, v70
	v_cvt_f32_f16_sdwa v45, v70 dst_sel:DWORD dst_unused:UNUSED_PAD src0_sel:WORD_1
	v_cvt_f32_f16_e32 v68, v71
	v_cvt_f32_f16_sdwa v69, v71 dst_sel:DWORD dst_unused:UNUSED_PAD src0_sel:WORD_1
	s_waitcnt vmcnt(20)
	v_cvt_f32_f16_e32 v38, v64
	v_cvt_f32_f16_sdwa v39, v64 dst_sel:DWORD dst_unused:UNUSED_PAD src0_sel:WORD_1
	v_cvt_f32_f16_e32 v42, v65
	v_cvt_f32_f16_sdwa v43, v65 dst_sel:DWORD dst_unused:UNUSED_PAD src0_sel:WORD_1
	v_cvt_f32_f16_e32 v36, v66
	v_cvt_f32_f16_sdwa v37, v66 dst_sel:DWORD dst_unused:UNUSED_PAD src0_sel:WORD_1
	v_cvt_f32_f16_e32 v40, v67
	v_cvt_f32_f16_sdwa v41, v67 dst_sel:DWORD dst_unused:UNUSED_PAD src0_sel:WORD_1
	v_pk_mul_f32 v[64:65], v[32:33], v[32:33]
	v_pk_mul_f32 v[66:67], v[34:35], v[34:35]
	v_pk_mul_f32 v[70:71], v[82:83], v[82:83]
	v_pk_mul_f32 v[86:87], v[84:85], v[84:85]
	v_pk_mul_f32 v[88:89], v[78:79], v[78:79]
	v_pk_mul_f32 v[90:91], v[80:81], v[80:81]
	v_add_f32_e32 v86, v86, v87
	v_add_f32_e32 v70, v70, v71
	v_add_f32_e32 v66, v66, v67
	v_add_f32_e32 v64, v64, v65
	v_add_f32_e32 v70, v70, v86
	v_add_f32_e32 v64, v64, v66
	v_add_f32_e32 v65, v90, v91
	v_add_f32_e32 v66, v88, v89
	v_pk_mul_f32 v[92:93], v[76:77], v[76:77]
	v_pk_mul_f32 v[94:95], v[74:75], v[74:75]
	v_add_f32_e32 v64, v64, v70
	v_add_f32_e32 v65, v66, v65
	v_add_f32_e32 v64, v64, v65
	v_add_f32_e32 v65, v94, v95
	v_add_f32_e32 v66, v92, v93
	v_pk_mul_f32 v[96:97], v[46:47], v[46:47]
	v_pk_mul_f32 v[98:99], v[72:73], v[72:73]
	v_add_f32_e32 v65, v66, v65
	v_add_f32_e32 v64, v65, v64
	v_add_f32_e32 v65, v98, v99
	v_add_f32_e32 v66, v96, v97
	v_pk_mul_f32 v[100:101], v[44:45], v[44:45]
	v_pk_mul_f32 v[102:103], v[68:69], v[68:69]
	v_add_f32_e32 v65, v66, v65
	v_add_f32_e32 v64, v65, v64
	v_add_f32_e32 v65, v102, v103
	v_add_f32_e32 v66, v100, v101
	v_pk_mul_f32 v[104:105], v[38:39], v[38:39]
	v_pk_mul_f32 v[106:107], v[42:43], v[42:43]
	v_add_f32_e32 v65, v66, v65
	v_add_f32_e32 v64, v65, v64
	v_add_f32_e32 v65, v106, v107
	v_add_f32_e32 v66, v104, v105
	v_pk_mul_f32 v[108:109], v[36:37], v[36:37]
	v_pk_mul_f32 v[110:111], v[40:41], v[40:41]
	v_add_f32_e32 v65, v66, v65
	v_add_f32_e32 v64, v65, v64
	v_add_f32_e32 v65, v110, v111
	v_add_f32_e32 v66, v108, v109
	v_add_f32_e32 v65, v66, v65
	v_add_f32_e32 v64, v65, v64
	s_nop 1
	v_add_f32_dpp v64, v64, v64 row_ror:8 row_mask:0xf bank_mask:0xf bound_ctrl:1
	s_nop 1
	v_add_f32_dpp v64, v64, v64 row_ror:4 row_mask:0xf bank_mask:0xf bound_ctrl:1
	s_nop 1
	v_add_f32_dpp v64, v64, v64 row_ror:2 row_mask:0xf bank_mask:0xf bound_ctrl:1
	s_nop 1
	v_add_f32_dpp v64, v64, v64 row_ror:1 row_mask:0xf bank_mask:0xf bound_ctrl:1
	ds_swizzle_b32 v65, v64 offset:swizzle(SWAP,16)
	s_waitcnt lgkmcnt(0)
	v_add_f32_e32 v64, v64, v65
	s_nop 0
	v_readlane_b32 s1, v64, 32
	v_readlane_b32 s0, v64, 0
	s_nop 0
	v_mov_b32_e32 v64, s1
	v_add_f32_e32 v64, s0, v64
	v_fmamk_f32 v64, v64, 0x3a000000, v238
	v_rsq_f32_e32 v64, v64
	s_movk_i32 s0, 0xf000
	v_pk_mul_f32 v[32:33], v[32:33], v[64:65] op_sel_hi:[1,0]
	v_pk_mul_f32 v[34:35], v[34:35], v[64:65] op_sel_hi:[1,0]
	v_pk_mul_f32 v[66:67], v[82:83], v[64:65] op_sel_hi:[1,0]
	v_pk_fma_f32 v[34:35], v[128:129], v[34:35], v[6:7]
	v_pk_fma_f32 v[32:33], v[130:131], v[32:33], v[4:5]
	v_pk_mul_f32 v[70:71], v[84:85], v[64:65] op_sel_hi:[1,0]
	v_pk_fma_f32 v[66:67], v[134:135], v[66:67], v[0:1]
	v_pk_fma_f32 v[70:71], v[132:133], v[70:71], v[2:3]
	v_cvt_pk_bf16_f32 v32, v32, v33
	v_cvt_pk_bf16_f32 v33, v34, v35
	v_cvt_pk_bf16_f32 v34, v66, v67
	v_add_co_u32_e32 v66, vcc, s0, v126
	v_cvt_pk_bf16_f32 v35, v70, v71
	s_nop 0
	v_addc_co_u32_e32 v67, vcc, -1, v127, vcc
	global_store_dwordx4 v[66:67], v[32:35], off offset:-3072
	v_pk_mul_f32 v[70:71], v[76:77], v[64:65] op_sel_hi:[1,0]
	v_pk_mul_f32 v[74:75], v[74:75], v[64:65] op_sel_hi:[1,0]
	v_pk_mul_f32 v[32:33], v[78:79], v[64:65] op_sel_hi:[1,0]
	v_pk_mul_f32 v[34:35], v[80:81], v[64:65] op_sel_hi:[1,0]
	v_pk_fma_f32 v[32:33], v[138:139], v[32:33], v[12:13]
	v_pk_fma_f32 v[34:35], v[136:137], v[34:35], v[14:15]
	v_pk_fma_f32 v[74:75], v[140:141], v[74:75], v[10:11]
	v_pk_fma_f32 v[70:71], v[142:143], v[70:71], v[8:9]
	v_cvt_pk_bf16_f32 v32, v32, v33
	v_cvt_pk_bf16_f32 v33, v34, v35
	v_cvt_pk_bf16_f32 v34, v70, v71
	v_cvt_pk_bf16_f32 v35, v74, v75
	global_store_dwordx4 v[66:67], v[32:35], off offset:-2048
	v_pk_mul_f32 v[44:45], v[44:45], v[64:65] op_sel_hi:[1,0]
	v_pk_mul_f32 v[36:37], v[36:37], v[64:65] op_sel_hi:[1,0]
	v_pk_mul_f32 v[32:33], v[46:47], v[64:65] op_sel_hi:[1,0]
	v_pk_mul_f32 v[34:35], v[72:73], v[64:65] op_sel_hi:[1,0]
	v_pk_mul_f32 v[46:47], v[68:69], v[64:65] op_sel_hi:[1,0]
	v_pk_fma_f32 v[34:35], v[144:145], v[34:35], v[22:23]
	v_pk_fma_f32 v[32:33], v[146:147], v[32:33], v[20:21]
	v_pk_fma_f32 v[46:47], v[148:149], v[46:47], v[18:19]
	v_pk_fma_f32 v[44:45], v[150:151], v[44:45], v[16:17]
	v_cvt_pk_bf16_f32 v32, v32, v33
	v_cvt_pk_bf16_f32 v33, v34, v35
	v_cvt_pk_bf16_f32 v34, v44, v45
	v_cvt_pk_bf16_f32 v35, v46, v47
	global_store_dwordx4 v[66:67], v[32:35], off offset:-1024
	v_pk_fma_f32 v[36:37], v[158:159], v[36:37], v[24:25]
	s_waitcnt vmcnt(17)
	v_cvt_f32_f16_e32 v44, v58
	v_pk_mul_f32 v[32:33], v[38:39], v[64:65] op_sel_hi:[1,0]
	v_pk_mul_f32 v[34:35], v[42:43], v[64:65] op_sel_hi:[1,0]
	v_pk_mul_f32 v[38:39], v[40:41], v[64:65] op_sel_hi:[1,0]
	v_pk_fma_f32 v[34:35], v[152:153], v[34:35], v[30:31]
	v_pk_fma_f32 v[32:33], v[154:155], v[32:33], v[28:29]
	v_pk_fma_f32 v[38:39], v[156:157], v[38:39], v[26:27]
	v_cvt_pk_bf16_f32 v32, v32, v33
	v_cvt_pk_bf16_f32 v33, v34, v35
	v_cvt_pk_bf16_f32 v34, v36, v37
	v_cvt_pk_bf16_f32 v35, v38, v39
	global_store_dwordx4 v[126:127], v[32:35], off offset:-4096
	v_cvt_f32_f16_e32 v36, v62
	v_cvt_f32_f16_sdwa v37, v62 dst_sel:DWORD dst_unused:UNUSED_PAD src0_sel:WORD_1
	v_cvt_f32_f16_e32 v32, v60
	v_cvt_f32_f16_sdwa v33, v60 dst_sel:DWORD dst_unused:UNUSED_PAD src0_sel:WORD_1
	v_cvt_f32_f16_e32 v34, v61
	v_cvt_f32_f16_sdwa v35, v61 dst_sel:DWORD dst_unused:UNUSED_PAD src0_sel:WORD_1
	v_cvt_f32_f16_e32 v38, v63
	v_cvt_f32_f16_sdwa v39, v63 dst_sel:DWORD dst_unused:UNUSED_PAD src0_sel:WORD_1
	v_cvt_f32_f16_e32 v40, v56
	v_cvt_f32_f16_sdwa v41, v56 dst_sel:DWORD dst_unused:UNUSED_PAD src0_sel:WORD_1
	v_cvt_f32_f16_e32 v42, v57
	v_cvt_f32_f16_sdwa v43, v57 dst_sel:DWORD dst_unused:UNUSED_PAD src0_sel:WORD_1
	v_cvt_f32_f16_sdwa v45, v58 dst_sel:DWORD dst_unused:UNUSED_PAD src0_sel:WORD_1
	v_cvt_f32_f16_e32 v46, v59
	v_cvt_f32_f16_sdwa v47, v59 dst_sel:DWORD dst_unused:UNUSED_PAD src0_sel:WORD_1
	v_pk_mul_f32 v[64:65], v[32:33], v[32:33]
	v_pk_mul_f32 v[66:67], v[34:35], v[34:35]
	v_pk_mul_f32 v[68:69], v[36:37], v[36:37]
	v_pk_mul_f32 v[70:71], v[38:39], v[38:39]
	s_waitcnt vmcnt(17)
	v_cvt_f32_f16_e32 v56, v52
	v_cvt_f32_f16_sdwa v57, v52 dst_sel:DWORD dst_unused:UNUSED_PAD src0_sel:WORD_1
	v_cvt_f32_f16_e32 v52, v53
	v_cvt_f32_f16_sdwa v53, v53 dst_sel:DWORD dst_unused:UNUSED_PAD src0_sel:WORD_1
	v_pk_mul_f32 v[72:73], v[40:41], v[40:41]
	v_pk_mul_f32 v[74:75], v[42:43], v[42:43]
	v_add_f32_e32 v70, v70, v71
	v_add_f32_e32 v68, v68, v69
	v_add_f32_e32 v66, v66, v67
	v_add_f32_e32 v64, v64, v65
	v_add_f32_e32 v68, v68, v70
	v_add_f32_e32 v64, v64, v66
	v_add_f32_e32 v65, v74, v75
	v_add_f32_e32 v66, v72, v73
	v_cvt_f32_f16_e32 v58, v54
	v_cvt_f32_f16_sdwa v59, v54 dst_sel:DWORD dst_unused:UNUSED_PAD src0_sel:WORD_1
	v_cvt_f32_f16_e32 v54, v55
	v_cvt_f32_f16_sdwa v55, v55 dst_sel:DWORD dst_unused:UNUSED_PAD src0_sel:WORD_1
	v_pk_mul_f32 v[76:77], v[44:45], v[44:45]
	v_pk_mul_f32 v[78:79], v[46:47], v[46:47]
	v_add_f32_e32 v64, v64, v68
	v_add_f32_e32 v65, v66, v65
	v_add_f32_e32 v64, v64, v65
	v_add_f32_e32 v65, v78, v79
	v_add_f32_e32 v66, v76, v77
	s_waitcnt vmcnt(16)
	v_cvt_f32_f16_e32 v60, v48
	v_cvt_f32_f16_sdwa v61, v48 dst_sel:DWORD dst_unused:UNUSED_PAD src0_sel:WORD_1
	v_cvt_f32_f16_e32 v48, v49
	v_cvt_f32_f16_sdwa v49, v49 dst_sel:DWORD dst_unused:UNUSED_PAD src0_sel:WORD_1
	v_pk_mul_f32 v[80:81], v[56:57], v[56:57]
	v_pk_mul_f32 v[82:83], v[52:53], v[52:53]
	v_add_f32_e32 v65, v66, v65
	v_add_f32_e32 v64, v65, v64
	v_add_f32_e32 v65, v82, v83
	v_add_f32_e32 v66, v80, v81
	v_cvt_f32_f16_e32 v62, v50
	v_cvt_f32_f16_sdwa v63, v50 dst_sel:DWORD dst_unused:UNUSED_PAD src0_sel:WORD_1
	v_cvt_f32_f16_e32 v50, v51
	v_cvt_f32_f16_sdwa v51, v51 dst_sel:DWORD dst_unused:UNUSED_PAD src0_sel:WORD_1
	v_pk_mul_f32 v[84:85], v[58:59], v[58:59]
	v_pk_mul_f32 v[86:87], v[54:55], v[54:55]
	v_add_f32_e32 v65, v66, v65
	v_add_f32_e32 v64, v65, v64
	v_add_f32_e32 v65, v86, v87
	v_add_f32_e32 v66, v84, v85
	v_pk_mul_f32 v[88:89], v[60:61], v[60:61]
	v_pk_mul_f32 v[90:91], v[48:49], v[48:49]
	v_add_f32_e32 v65, v66, v65
	v_add_f32_e32 v64, v65, v64
	v_add_f32_e32 v65, v90, v91
	v_add_f32_e32 v66, v88, v89
	v_pk_mul_f32 v[92:93], v[62:63], v[62:63]
	v_pk_mul_f32 v[94:95], v[50:51], v[50:51]
	v_add_f32_e32 v65, v66, v65
	v_add_f32_e32 v64, v65, v64
	v_add_f32_e32 v65, v94, v95
	v_add_f32_e32 v66, v92, v93
	v_add_f32_e32 v65, v66, v65
	v_add_f32_e32 v64, v65, v64
	s_nop 1
	v_add_f32_dpp v64, v64, v64 row_ror:8 row_mask:0xf bank_mask:0xf bound_ctrl:1
	s_nop 1
	v_add_f32_dpp v64, v64, v64 row_ror:4 row_mask:0xf bank_mask:0xf bound_ctrl:1
	s_nop 1
	v_add_f32_dpp v64, v64, v64 row_ror:2 row_mask:0xf bank_mask:0xf bound_ctrl:1
	s_nop 1
	v_add_f32_dpp v64, v64, v64 row_ror:1 row_mask:0xf bank_mask:0xf bound_ctrl:1
	ds_swizzle_b32 v65, v64 offset:swizzle(SWAP,16)
	s_waitcnt lgkmcnt(0)
	v_add_f32_e32 v64, v64, v65
	s_nop 0
	v_readlane_b32 s1, v64, 32
	v_readlane_b32 s0, v64, 0
	s_nop 0
	v_mov_b32_e32 v64, s1
	v_add_f32_e32 v64, s0, v64
	v_fmamk_f32 v64, v64, 0x3a000000, v238
	v_rsq_f32_e32 v64, v64
	s_nop 0
	v_pk_mul_f32 v[32:33], v[32:33], v[64:65] op_sel_hi:[1,0]
	v_pk_mul_f32 v[34:35], v[34:35], v[64:65] op_sel_hi:[1,0]
	v_pk_fma_f32 v[4:5], v[130:131], v[32:33], v[4:5]
	v_pk_fma_f32 v[6:7], v[128:129], v[34:35], v[6:7]
	v_pk_mul_f32 v[32:33], v[36:37], v[64:65] op_sel_hi:[1,0]
	v_pk_mul_f32 v[34:35], v[38:39], v[64:65] op_sel_hi:[1,0]
	s_nop 0
	v_pk_fma_f32 v[34:35], v[132:133], v[34:35], v[2:3]
	v_pk_fma_f32 v[2:3], v[134:135], v[32:33], v[0:1]
	v_cvt_pk_bf16_f32 v0, v4, v5
	v_cvt_pk_bf16_f32 v1, v6, v7
	v_cvt_pk_bf16_f32 v2, v2, v3
	v_cvt_pk_bf16_f32 v3, v34, v35
	global_store_dwordx4 v[126:127], v[0:3], off offset:-3072
	v_pk_mul_f32 v[4:5], v[44:45], v[64:65] op_sel_hi:[1,0]
	v_pk_mul_f32 v[6:7], v[46:47], v[64:65] op_sel_hi:[1,0]
	v_pk_mul_f32 v[0:1], v[40:41], v[64:65] op_sel_hi:[1,0]
	v_pk_mul_f32 v[2:3], v[42:43], v[64:65] op_sel_hi:[1,0]
	v_pk_fma_f32 v[0:1], v[138:139], v[0:1], v[12:13]
	v_pk_fma_f32 v[2:3], v[136:137], v[2:3], v[14:15]
	v_pk_fma_f32 v[6:7], v[140:141], v[6:7], v[10:11]
	v_pk_fma_f32 v[4:5], v[142:143], v[4:5], v[8:9]
	v_cvt_pk_bf16_f32 v0, v0, v1
	v_cvt_pk_bf16_f32 v1, v2, v3
	v_cvt_pk_bf16_f32 v2, v4, v5
	v_cvt_pk_bf16_f32 v3, v6, v7
	global_store_dwordx4 v[126:127], v[0:3], off offset:-2048
	v_pk_mul_f32 v[4:5], v[58:59], v[64:65] op_sel_hi:[1,0]
	v_pk_mul_f32 v[6:7], v[54:55], v[64:65] op_sel_hi:[1,0]
	v_pk_mul_f32 v[0:1], v[56:57], v[64:65] op_sel_hi:[1,0]
	v_pk_mul_f32 v[2:3], v[52:53], v[64:65] op_sel_hi:[1,0]
	v_pk_fma_f32 v[0:1], v[146:147], v[0:1], v[20:21]
	v_pk_fma_f32 v[2:3], v[144:145], v[2:3], v[22:23]
	v_pk_fma_f32 v[6:7], v[148:149], v[6:7], v[18:19]
	v_pk_fma_f32 v[4:5], v[150:151], v[4:5], v[16:17]
	v_cvt_pk_bf16_f32 v0, v0, v1
	v_cvt_pk_bf16_f32 v1, v2, v3
	v_cvt_pk_bf16_f32 v2, v4, v5
	v_cvt_pk_bf16_f32 v3, v6, v7
	global_store_dwordx4 v[126:127], v[0:3], off offset:-1024
	v_pk_mul_f32 v[4:5], v[62:63], v[64:65] op_sel_hi:[1,0]
	v_pk_mul_f32 v[6:7], v[50:51], v[64:65] op_sel_hi:[1,0]
	v_pk_mul_f32 v[0:1], v[60:61], v[64:65] op_sel_hi:[1,0]
	v_pk_mul_f32 v[2:3], v[48:49], v[64:65] op_sel_hi:[1,0]
	v_pk_fma_f32 v[0:1], v[154:155], v[0:1], v[28:29]
	v_pk_fma_f32 v[2:3], v[152:153], v[2:3], v[30:31]
	v_pk_fma_f32 v[6:7], v[156:157], v[6:7], v[26:27]
	v_pk_fma_f32 v[4:5], v[158:159], v[4:5], v[24:25]
	v_cvt_pk_bf16_f32 v0, v0, v1
	v_cvt_pk_bf16_f32 v1, v2, v3
	v_cvt_pk_bf16_f32 v2, v4, v5
	v_cvt_pk_bf16_f32 v3, v6, v7
	global_store_dwordx4 v[126:127], v[0:3], off
	v_lshl_add_u64 v[126:127], v[126:127], 0, s[42:43]
	s_cbranch_scc1 .LBB0_218
